# s26
# speedup vs baseline: 1.0188x; 1.0066x over previous
.LBB1_5:
	v_lshlrev_b32_e32 v67, 4, v1
	v_lshrrev_b32_e32 v1, 1, v1
	v_lshrrev_b32_e32 v69, 5, v132
	v_ashrrev_i32_e32 v66, 4, v132
	v_bitop3_b32 v1, v1, v69, 7 bitop3:0x78
	s_add_u32 s22, s24, s2
	v_lshlrev_b32_e32 v68, 7, v66
	v_lshlrev_b32_e32 v1, 4, v1
	v_and_b32_e32 v0, 8, v0
	s_addc_u32 s90, s25, s3
	v_lshl_or_b32 v201, v66, 12, v67
	v_or3_b32 v0, v68, v1, v0
	v_add_u32_e32 v100, 0x10000, v0
	v_cvt_pk_f16_f32 v1, v64, v65
	v_cvt_pk_f16_f32 v0, v62, v63
	v_cvt_pk_f16_f32 v61, v60, v61
	v_cvt_pk_f16_f32 v60, v58, v59
	ds_write2st64_b64 v100, v[0:1], v[60:61] offset1:8
	v_cvt_pk_f16_f32 v1, v56, v57
	v_cvt_pk_f16_f32 v0, v54, v55
	v_cvt_pk_f16_f32 v53, v52, v53
	v_cvt_pk_f16_f32 v52, v50, v51
	ds_write2st64_b64 v100, v[0:1], v[52:53] offset0:16 offset1:24
	v_cvt_pk_f16_f32 v1, v48, v49
	v_cvt_pk_f16_f32 v0, v46, v47
	v_cvt_pk_f16_f32 v45, v44, v45
	v_cvt_pk_f16_f32 v44, v42, v43
	ds_write2st64_b64 v100, v[0:1], v[44:45] offset0:32 offset1:40
	v_cvt_pk_f16_f32 v1, v40, v41
	v_cvt_pk_f16_f32 v0, v38, v39
	v_cvt_pk_f16_f32 v37, v36, v37
	v_cvt_pk_f16_f32 v36, v34, v35
	ds_write2st64_b64 v100, v[0:1], v[36:37] offset0:48 offset1:56
	s_add_u32 s0, s22, 0x200
	s_addc_u32 s1, s90, 0
	s_add_u32 s70, s0, 0x20000
	s_addc_u32 s71, s1, 0
	s_add_u32 s72, s0, 0x40000
	s_addc_u32 s73, s1, 0
	s_add_u32 s92, s0, 0x60000
	s_addc_u32 s93, s1, 0
	s_add_u32 s94, s0, 0x80000
	s_addc_u32 s95, s1, 0
	s_add_u32 s96, s0, 0xa0000
	s_addc_u32 s97, s1, 0
	s_add_u32 s98, s0, 0xc0000
	s_addc_u32 s99, s1, 0
	s_add_u32 s80, s0, 0xe0000
	s_addc_u32 s81, s1, 0
	global_load_dwordx4 v[70:73], v201, s[0:1] nt
	global_load_dwordx4 v[42:45], v201, s[70:71] nt
	global_load_dwordx4 v[46:49], v201, s[72:73] nt
	global_load_dwordx4 v[66:69], v201, s[92:93] nt
	global_load_dwordx4 v[62:65], v201, s[94:95] nt
	global_load_dwordx4 v[58:61], v201, s[96:97] nt
	global_load_dwordx4 v[54:57], v201, s[98:99] nt
	global_load_dwordx4 v[50:53], v201, s[80:81] nt
	s_waitcnt vmcnt(8)
	s_waitcnt lgkmcnt(0)
	s_barrier
	ds_read_b128 v[34:37], v131
	ds_read_b128 v[38:41], v131 offset:2048
	ds_read_b128 v[74:77], v131 offset:4096
	ds_read_b128 v[78:81], v131 offset:6144
	ds_read_b128 v[82:85], v129
	ds_read_b128 v[86:89], v129 offset:2048
	s_add_u32 s70, s22, 0x300
	v_add_u32_e32 v95, 0x8000, v94
	v_lshl_add_u64 v[0:1], s[26:27], 0, v[196:197]
	s_addc_u32 s71, s90, 0
	v_readfirstlane_b32 s0, v95
	s_mov_b32 m0, s0
	v_cvt_pk_f16_f32 v33, v32, v33
	global_load_lds_dwordx4 v[0:1], off
	v_cvt_pk_f16_f32 v32, v30, v31
	ds_write_b64 v100, v[32:33] offset:32768
	global_load_dwordx4 v[30:33], v201, s[70:71] nt
	s_setprio 1
	s_waitcnt lgkmcnt(1)
	v_mfma_f32_16x16x32_f16 v[90:93], v[82:85], v[34:37], 0
	v_mfma_f32_16x16x32_f16 v[102:105], v[82:85], v[38:41], 0
	v_mfma_f32_16x16x32_f16 v[106:109], v[82:85], v[74:77], 0
	v_mfma_f32_16x16x32_f16 v[82:85], v[82:85], v[78:81], 0
	v_mfma_f32_16x16x32_f16 v[110:113], v[86:89], v[34:37], 0
	v_mfma_f32_16x16x32_f16 v[114:117], v[86:89], v[38:41], 0
	v_mfma_f32_16x16x32_f16 v[118:121], v[86:89], v[74:77], 0
	v_mfma_f32_16x16x32_f16 v[86:89], v[86:89], v[78:81], 0
	s_setprio 0
	ds_read_b128 v[122:125], v129 offset:4096
	ds_read_b128 v[134:137], v129 offset:6144
	v_add_u32_e32 v96, 0xa000, v94
	v_lshl_add_u64 v[98:99], v[0:1], 0, s[58:59]
	v_readfirstlane_b32 s1, v96
	s_mov_b32 m0, s1
	v_cvt_pk_f16_f32 v29, v28, v29
	global_load_lds_dwordx4 v[98:99], off
	v_cvt_pk_f16_f32 v28, v26, v27
	ds_write_b64 v100, v[28:29] offset:36864
	s_add_u32 s70, s22, 0x20300
	s_addc_u32 s71, s90, 0
	global_load_dwordx4 v[26:29], v201, s[70:71] nt
	s_setprio 1
	s_waitcnt lgkmcnt(1)
	v_mfma_f32_16x16x32_f16 v[138:141], v[122:125], v[34:37], 0
	v_mfma_f32_16x16x32_f16 v[142:145], v[122:125], v[38:41], 0
	v_mfma_f32_16x16x32_f16 v[146:149], v[122:125], v[74:77], 0
	v_mfma_f32_16x16x32_f16 v[122:125], v[122:125], v[78:81], 0
	v_mfma_f32_16x16x32_f16 v[150:153], v[134:137], v[34:37], 0
	v_mfma_f32_16x16x32_f16 v[154:157], v[134:137], v[38:41], 0
	v_mfma_f32_16x16x32_f16 v[158:161], v[134:137], v[74:77], 0
	v_mfma_f32_16x16x32_f16 v[134:137], v[134:137], v[78:81], 0
	s_setprio 0
	ds_read_b128 v[162:165], v129 offset:8192
	ds_read_b128 v[166:169], v129 offset:10240
	v_add_u32_e32 v97, 0xc000, v94
	v_lshl_add_u64 v[98:99], v[0:1], 0, s[60:61]
	v_readfirstlane_b32 s71, v97
	s_mov_b32 m0, s71
	v_cvt_pk_f16_f32 v25, v24, v25
	global_load_lds_dwordx4 v[98:99], off
	v_cvt_pk_f16_f32 v24, v22, v23
	ds_write_b64 v100, v[24:25] offset:40960
	s_add_u32 s72, s22, 0x40300
	s_addc_u32 s73, s90, 0
	global_load_dwordx4 v[22:25], v201, s[72:73] nt
	s_setprio 1
	s_waitcnt lgkmcnt(1)
	v_mfma_f32_16x16x32_f16 v[170:173], v[162:165], v[34:37], 0
	v_mfma_f32_16x16x32_f16 v[174:177], v[162:165], v[38:41], 0
	v_mfma_f32_16x16x32_f16 v[178:181], v[162:165], v[74:77], 0
	v_mfma_f32_16x16x32_f16 v[162:165], v[162:165], v[78:81], 0
	v_mfma_f32_16x16x32_f16 v[182:185], v[166:169], v[34:37], 0
	v_mfma_f32_16x16x32_f16 v[186:189], v[166:169], v[38:41], 0
	v_mfma_f32_16x16x32_f16 v[190:193], v[166:169], v[74:77], 0
	v_mfma_f32_16x16x32_f16 v[166:169], v[166:169], v[78:81], 0
	s_setprio 0
	ds_read_b128 v[202:205], v129 offset:12288
	ds_read_b128 v[206:209], v129 offset:14336
	v_add_u32_e32 v98, 0xe000, v94
	v_lshl_add_u64 v[0:1], v[0:1], 0, s[62:63]
	v_readfirstlane_b32 s72, v98
	s_mov_b32 m0, s72
	s_nop 0
	global_load_lds_dwordx4 v[0:1], off
	v_cvt_pk_f16_f32 v1, v20, v21
	v_cvt_pk_f16_f32 v0, v18, v19
	ds_write_b64 v100, v[0:1] offset:45056
	s_add_u32 s80, s22, 0x60300
	s_addc_u32 s81, s90, 0
	global_load_dwordx4 v[18:21], v201, s[80:81] nt
	s_setprio 1
	s_waitcnt lgkmcnt(1)
	v_mfma_f32_16x16x32_f16 v[210:213], v[202:205], v[34:37], 0
	v_mfma_f32_16x16x32_f16 v[214:217], v[202:205], v[38:41], 0
	v_mfma_f32_16x16x32_f16 v[218:221], v[202:205], v[74:77], 0
	v_mfma_f32_16x16x32_f16 v[202:205], v[202:205], v[78:81], 0
	v_mfma_f32_16x16x32_f16 v[74:77], v[206:209], v[74:77], 0
	v_mfma_f32_16x16x32_f16 v[78:81], v[206:209], v[78:81], 0
	v_mfma_f32_16x16x32_f16 v[222:225], v[206:209], v[34:37], 0
	v_mfma_f32_16x16x32_f16 v[226:229], v[206:209], v[38:41], 0
	s_setprio 0
	ds_read_b128 v[206:209], v128
	ds_read_b128 v[230:233], v128 offset:2048
	ds_read_b128 v[234:237], v128 offset:4096
	ds_read_b128 v[238:241], v128 offset:6144
	ds_read_b128 v[34:37], v130
	ds_read_b128 v[38:41], v130 offset:2048
	v_cvt_pk_f16_f32 v1, v16, v17
	v_cvt_pk_f16_f32 v0, v14, v15
	ds_write_b64 v100, v[0:1] offset:49152
	s_add_u32 s80, s22, 0x80300
	s_addc_u32 s81, s90, 0
	global_load_dwordx4 v[14:17], v201, s[80:81] nt
	s_setprio 1
	s_waitcnt lgkmcnt(1)
	v_mfma_f32_16x16x32_f16 v[90:93], v[34:37], v[206:209], v[90:93]
	v_mfma_f32_16x16x32_f16 v[102:105], v[34:37], v[230:233], v[102:105]
	v_mfma_f32_16x16x32_f16 v[106:109], v[34:37], v[234:237], v[106:109]
	v_mfma_f32_16x16x32_f16 v[82:85], v[34:37], v[238:241], v[82:85]
	v_mfma_f32_16x16x32_f16 v[110:113], v[38:41], v[206:209], v[110:113]
	v_mfma_f32_16x16x32_f16 v[114:117], v[38:41], v[230:233], v[114:117]
	v_mfma_f32_16x16x32_f16 v[118:121], v[38:41], v[234:237], v[118:121]
	v_mfma_f32_16x16x32_f16 v[86:89], v[38:41], v[238:241], v[86:89]
	s_setprio 0
	ds_read_b128 v[34:37], v130 offset:4096
	ds_read_b128 v[38:41], v130 offset:6144
	v_cvt_pk_f16_f32 v1, v12, v13
	v_cvt_pk_f16_f32 v0, v10, v11
	ds_write_b64 v100, v[0:1] offset:53248
	s_add_u32 s80, s22, 0xa0300
	s_addc_u32 s81, s90, 0
	global_load_dwordx4 v[10:13], v201, s[80:81] nt
	s_setprio 1
	s_waitcnt lgkmcnt(1)
	v_mfma_f32_16x16x32_f16 v[146:149], v[34:37], v[234:237], v[146:149]
	v_mfma_f32_16x16x32_f16 v[122:125], v[34:37], v[238:241], v[122:125]
	v_mfma_f32_16x16x32_f16 v[134:137], v[38:41], v[238:241], v[134:137]
	v_mfma_f32_16x16x32_f16 v[138:141], v[34:37], v[206:209], v[138:141]
	v_mfma_f32_16x16x32_f16 v[142:145], v[34:37], v[230:233], v[142:145]
	v_mfma_f32_16x16x32_f16 v[150:153], v[38:41], v[206:209], v[150:153]
	v_mfma_f32_16x16x32_f16 v[154:157], v[38:41], v[230:233], v[154:157]
	v_mfma_f32_16x16x32_f16 v[158:161], v[38:41], v[234:237], v[158:161]
	s_setprio 0
	ds_read_b128 v[38:41], v130 offset:8192
	ds_read_b128 v[242:245], v130 offset:10240
	v_cvt_pk_f16_f32 v1, v8, v9
	v_cvt_pk_f16_f32 v0, v6, v7
	ds_write_b64 v100, v[0:1] offset:57344
	s_add_u32 s80, s22, 0xc0300
	s_addc_u32 s81, s90, 0
	global_load_dwordx4 v[34:37], v201, s[80:81] nt
	s_setprio 1
	s_waitcnt lgkmcnt(1)
	v_mfma_f32_16x16x32_f16 v[6:9], v[38:41], v[206:209], v[170:173]
	v_mfma_f32_16x16x32_f16 v[170:173], v[38:41], v[230:233], v[174:177]
	v_mfma_f32_16x16x32_f16 v[174:177], v[38:41], v[234:237], v[178:181]
	v_mfma_f32_16x16x32_f16 v[162:165], v[38:41], v[238:241], v[162:165]
	v_mfma_f32_16x16x32_f16 v[178:181], v[242:245], v[206:209], v[182:185]
	v_mfma_f32_16x16x32_f16 v[182:185], v[242:245], v[230:233], v[186:189]
	v_mfma_f32_16x16x32_f16 v[186:189], v[242:245], v[234:237], v[190:193]
	v_mfma_f32_16x16x32_f16 v[166:169], v[242:245], v[238:241], v[166:169]
	s_setprio 0
	s_nop 0
	ds_read_b128 v[190:193], v130 offset:12288
	ds_read_b128 v[242:245], v130 offset:14336
	v_cvt_pk_f16_f32 v1, v4, v5
	v_cvt_pk_f16_f32 v0, v2, v3
	ds_write_b64 v100, v[0:1] offset:61440
	s_add_u32 s80, s22, 0xe0300
	s_addc_u32 s81, s90, 0
	global_load_dwordx4 v[38:41], v201, s[80:81] nt
	s_setprio 1
	s_waitcnt lgkmcnt(1)
	v_mfma_f32_16x16x32_f16 v[78:81], v[242:245], v[238:241], v[78:81]
	v_mfma_f32_16x16x32_f16 v[210:213], v[190:193], v[206:209], v[210:213]
	v_mfma_f32_16x16x32_f16 v[214:217], v[190:193], v[230:233], v[214:217]
	v_mfma_f32_16x16x32_f16 v[218:221], v[190:193], v[234:237], v[218:221]
	v_mfma_f32_16x16x32_f16 v[190:193], v[190:193], v[238:241], v[202:205]
	v_mfma_f32_16x16x32_f16 v[202:205], v[242:245], v[206:209], v[222:225]
	v_mfma_f32_16x16x32_f16 v[206:209], v[242:245], v[230:233], v[226:229]
	v_mfma_f32_16x16x32_f16 v[222:225], v[242:245], v[234:237], v[74:77]
	s_setprio 0
	s_waitcnt vmcnt(5)
	s_waitcnt lgkmcnt(0)
	s_barrier
	ds_read_b128 v[226:229], v131 offset:32768
	ds_read_b128 v[230:233], v131 offset:34816
	ds_read_b128 v[234:237], v131 offset:36864
	ds_read_b128 v[238:241], v131 offset:38912
	ds_read_b128 v[74:77], v129 offset:32768
	ds_read_b128 v[242:245], v129 offset:34816
	s_add_u32 s80, s22, 0x400
	s_addc_u32 s81, s90, 0
	v_lshl_add_u64 v[198:199], s[28:29], 0, v[196:197]
	v_readfirstlane_b32 s70, v94
	s_mov_b32 m0, s70
	v_cvt_pk_f16_f32 v1, v72, v73
	global_load_lds_dwordx4 v[198:199], off
	v_cvt_pk_f16_f32 v0, v70, v71
	ds_write_b64 v100, v[0:1]
	global_load_dwordx4 v[0:3], v201, s[80:81] nt
	s_setprio 1
	s_waitcnt lgkmcnt(1)
	v_mfma_f32_16x16x32_f16 v[70:73], v[74:77], v[226:229], v[90:93]
	v_mfma_f32_16x16x32_f16 v[90:93], v[74:77], v[230:233], v[102:105]
	v_mfma_f32_16x16x32_f16 v[104:107], v[74:77], v[234:237], v[106:109]
	v_mfma_f32_16x16x32_f16 v[82:85], v[74:77], v[238:241], v[82:85]
	v_mfma_f32_16x16x32_f16 v[108:111], v[242:245], v[226:229], v[110:113]
	v_mfma_f32_16x16x32_f16 v[112:115], v[242:245], v[230:233], v[114:117]
	v_mfma_f32_16x16x32_f16 v[116:119], v[242:245], v[234:237], v[118:121]
	v_mfma_f32_16x16x32_f16 v[86:89], v[242:245], v[238:241], v[86:89]
	s_setprio 0
	ds_read_b128 v[74:77], v129 offset:36864
	ds_read_b128 v[242:245], v129 offset:38912
	v_add_u32_e32 v99, 0x2000, v94
	v_lshl_add_u64 v[4:5], v[198:199], 0, s[58:59]
	v_readfirstlane_b32 s73, v99
	s_mov_b32 m0, s73
	s_nop 0
	global_load_lds_dwordx4 v[4:5], off
	v_cvt_pk_f16_f32 v5, v44, v45
	v_cvt_pk_f16_f32 v4, v42, v43
	ds_write_b64 v100, v[4:5] offset:4096
	s_add_u32 s80, s22, 0x20400
	s_addc_u32 s81, s90, 0
	global_load_dwordx4 v[42:45], v201, s[80:81] nt
	s_setprio 1
	s_waitcnt lgkmcnt(1)
	v_mfma_f32_16x16x32_f16 v[146:149], v[74:77], v[234:237], v[146:149]
	v_mfma_f32_16x16x32_f16 v[120:123], v[74:77], v[238:241], v[122:125]
	v_mfma_f32_16x16x32_f16 v[124:127], v[242:245], v[226:229], v[150:153]
	v_mfma_f32_16x16x32_f16 v[134:137], v[242:245], v[238:241], v[134:137]
	v_mfma_f32_16x16x32_f16 v[138:141], v[74:77], v[226:229], v[138:141]
	v_mfma_f32_16x16x32_f16 v[142:145], v[74:77], v[230:233], v[142:145]
	v_mfma_f32_16x16x32_f16 v[150:153], v[242:245], v[230:233], v[154:157]
	v_mfma_f32_16x16x32_f16 v[154:157], v[242:245], v[234:237], v[158:161]
	s_setprio 0
	ds_read_b128 v[74:77], v129 offset:40960
	s_nop 0
	ds_read_b128 v[158:161], v129 offset:43008
	v_add_u32_e32 v101, 0x4000, v94
	v_lshl_add_u64 v[4:5], v[198:199], 0, s[60:61]
	v_readfirstlane_b32 s91, v101
	s_mov_b32 m0, s91
	s_nop 0
	global_load_lds_dwordx4 v[4:5], off
	v_cvt_pk_f16_f32 v5, v48, v49
	v_cvt_pk_f16_f32 v4, v46, v47
	ds_write_b64 v100, v[4:5] offset:8192
	s_add_u32 s80, s22, 0x40400
	s_addc_u32 s81, s90, 0
	global_load_dwordx4 v[46:49], v201, s[80:81] nt
	s_setprio 1
	s_waitcnt lgkmcnt(1)
	v_mfma_f32_16x16x32_f16 v[4:7], v[74:77], v[226:229], v[6:9]
	v_mfma_f32_16x16x32_f16 v[170:173], v[74:77], v[230:233], v[170:173]
	v_mfma_f32_16x16x32_f16 v[174:177], v[74:77], v[234:237], v[174:177]
	v_mfma_f32_16x16x32_f16 v[162:165], v[74:77], v[238:241], v[162:165]
	v_mfma_f32_16x16x32_f16 v[178:181], v[158:161], v[226:229], v[178:181]
	v_mfma_f32_16x16x32_f16 v[182:185], v[158:161], v[230:233], v[182:185]
	v_mfma_f32_16x16x32_f16 v[186:189], v[158:161], v[234:237], v[186:189]
	v_mfma_f32_16x16x32_f16 v[158:161], v[158:161], v[238:241], v[166:169]
	s_setprio 0
	s_nop 1
	ds_read_b128 v[166:169], v129 offset:45056
	ds_read_b128 v[242:245], v129 offset:47104
	v_add_u32_e32 v102, 0x6000, v94
	v_lshl_add_u64 v[8:9], v[198:199], 0, s[62:63]
	v_readfirstlane_b32 s92, v102
	s_mov_b32 m0, s92
	s_nop 0
	global_load_lds_dwordx4 v[8:9], off
	v_cvt_pk_f16_f32 v9, v68, v69
	v_cvt_pk_f16_f32 v8, v66, v67
	ds_write_b64 v100, v[8:9] offset:12288
	s_add_u32 s80, s22, 0x60400
	s_addc_u32 s81, s90, 0
	global_load_dwordx4 v[74:77], v201, s[80:81] nt
	s_setprio 1
	s_waitcnt lgkmcnt(1)
	v_mfma_f32_16x16x32_f16 v[66:69], v[166:169], v[226:229], v[210:213]
	v_mfma_f32_16x16x32_f16 v[210:213], v[166:169], v[230:233], v[214:217]
	v_mfma_f32_16x16x32_f16 v[214:217], v[166:169], v[234:237], v[218:221]
	v_mfma_f32_16x16x32_f16 v[166:169], v[166:169], v[238:241], v[190:193]
	v_mfma_f32_16x16x32_f16 v[190:193], v[242:245], v[226:229], v[202:205]
	v_mfma_f32_16x16x32_f16 v[202:205], v[242:245], v[230:233], v[206:209]
	v_mfma_f32_16x16x32_f16 v[206:209], v[242:245], v[234:237], v[222:225]
	v_mfma_f32_16x16x32_f16 v[218:221], v[242:245], v[238:241], v[78:81]
	s_setprio 0
	s_nop 0
	ds_read_b128 v[222:225], v128 offset:32768
	ds_read_b128 v[226:229], v128 offset:34816
	ds_read_b128 v[230:233], v128 offset:36864
	ds_read_b128 v[234:237], v128 offset:38912
	ds_read_b128 v[238:241], v130 offset:32768
	ds_read_b128 v[242:245], v130 offset:34816
	v_cvt_pk_f16_f32 v9, v64, v65
	v_cvt_pk_f16_f32 v8, v62, v63
	ds_write_b64 v100, v[8:9] offset:16384
	s_add_u32 s80, s22, 0x80400
	s_addc_u32 s81, s90, 0
	global_load_dwordx4 v[78:81], v201, s[80:81] nt
	s_setprio 1
	s_waitcnt lgkmcnt(1)
	v_mfma_f32_16x16x32_f16 v[62:65], v[238:241], v[222:225], v[70:73]
	v_mfma_f32_16x16x32_f16 v[70:73], v[238:241], v[226:229], v[90:93]
	v_mfma_f32_16x16x32_f16 v[104:107], v[238:241], v[230:233], v[104:107]
	v_mfma_f32_16x16x32_f16 v[108:111], v[242:245], v[222:225], v[108:111]
	v_mfma_f32_16x16x32_f16 v[112:115], v[242:245], v[226:229], v[112:115]
	v_mfma_f32_16x16x32_f16 v[116:119], v[242:245], v[230:233], v[116:119]
	v_mfma_f32_16x16x32_f16 v[238:241], v[238:241], v[234:237], v[82:85]
	v_mfma_f32_16x16x32_f16 v[242:245], v[242:245], v[234:237], v[86:89]
	s_setprio 0
	s_nop 1
	ds_read_b128 v[86:89], v130 offset:36864
	ds_read_b128 v[90:93], v130 offset:38912
	v_cvt_pk_f16_f32 v9, v60, v61
	v_cvt_pk_f16_f32 v8, v58, v59
	ds_write_b64 v100, v[8:9] offset:20480
	s_add_u32 s80, s22, 0xa0400
	s_addc_u32 s81, s90, 0
	global_load_dwordx4 v[82:85], v201, s[80:81] nt
	s_setprio 1
	s_waitcnt lgkmcnt(1)
	v_mfma_f32_16x16x32_f16 v[58:61], v[86:89], v[222:225], v[138:141]
	v_mfma_f32_16x16x32_f16 v[138:141], v[86:89], v[226:229], v[142:145]
	v_mfma_f32_16x16x32_f16 v[142:145], v[86:89], v[230:233], v[146:149]
	v_mfma_f32_16x16x32_f16 v[120:123], v[86:89], v[234:237], v[120:123]
	v_mfma_f32_16x16x32_f16 v[124:127], v[90:93], v[222:225], v[124:127]
	v_mfma_f32_16x16x32_f16 v[146:149], v[90:93], v[226:229], v[150:153]
	v_mfma_f32_16x16x32_f16 v[134:137], v[90:93], v[234:237], v[134:137]
	v_mfma_f32_16x16x32_f16 v[150:153], v[90:93], v[230:233], v[154:157]
	s_setprio 0
	ds_read_b128 v[90:93], v130 offset:40960
	s_nop 0
	ds_read_b128 v[154:157], v130 offset:43008
	v_cvt_pk_f16_f32 v9, v56, v57
	v_cvt_pk_f16_f32 v8, v54, v55
	ds_write_b64 v100, v[8:9] offset:24576
	s_add_u32 s80, s22, 0xc0400
	s_addc_u32 s81, s90, 0
	global_load_dwordx4 v[86:89], v201, s[80:81] nt
	s_setprio 1
	s_waitcnt lgkmcnt(1)
	v_mfma_f32_16x16x32_f16 v[246:249], v[90:93], v[222:225], v[4:7]
	v_mfma_f32_16x16x32_f16 v[170:173], v[90:93], v[226:229], v[170:173]
	v_mfma_f32_16x16x32_f16 v[174:177], v[90:93], v[230:233], v[174:177]
	v_mfma_f32_16x16x32_f16 v[162:165], v[90:93], v[234:237], v[162:165]
	v_mfma_f32_16x16x32_f16 v[178:181], v[154:157], v[222:225], v[178:181]
	v_mfma_f32_16x16x32_f16 v[182:185], v[154:157], v[226:229], v[182:185]
	v_mfma_f32_16x16x32_f16 v[186:189], v[154:157], v[230:233], v[186:189]
	v_mfma_f32_16x16x32_f16 v[154:157], v[154:157], v[234:237], v[158:161]
	s_setprio 0
	ds_read_b128 v[4:7], v130 offset:45056
	ds_read_b128 v[54:57], v130 offset:47104
	v_cvt_pk_f16_f32 v9, v52, v53
	v_cvt_pk_f16_f32 v8, v50, v51
	ds_write_b64 v100, v[8:9] offset:28672
	s_add_u32 s80, s22, 0xe0400
	s_addc_u32 s81, s90, 0
	global_load_dwordx4 v[90:93], v201, s[80:81] nt
	s_setprio 1
	s_waitcnt lgkmcnt(1)
	v_mfma_f32_16x16x32_f16 v[66:69], v[4:7], v[222:225], v[66:69]
	v_mfma_f32_16x16x32_f16 v[158:161], v[4:7], v[226:229], v[210:213]
	v_mfma_f32_16x16x32_f16 v[210:213], v[4:7], v[230:233], v[214:217]
	v_mfma_f32_16x16x32_f16 v[166:169], v[4:7], v[234:237], v[166:169]
	v_mfma_f32_16x16x32_f16 v[190:193], v[54:57], v[222:225], v[190:193]
	v_mfma_f32_16x16x32_f16 v[202:205], v[54:57], v[226:229], v[202:205]
	v_mfma_f32_16x16x32_f16 v[206:209], v[54:57], v[230:233], v[206:209]
	v_mfma_f32_16x16x32_f16 v[214:217], v[54:57], v[234:237], v[218:221]
	s_setprio 0
	s_waitcnt vmcnt(5)
	s_waitcnt lgkmcnt(0)
	s_barrier
	s_nop 0
	ds_read_b128 v[218:221], v131
	ds_read_b128 v[222:225], v131 offset:2048
	ds_read_b128 v[226:229], v131 offset:4096
	ds_read_b128 v[230:233], v131 offset:6144
	ds_read_b128 v[50:53], v129
	ds_read_b128 v[54:57], v129 offset:2048
	s_add_u32 s80, s22, 0x500
	v_lshl_add_u64 v[8:9], s[30:31], 0, v[196:197]
	s_addc_u32 s81, s90, 0
	s_mov_b32 m0, s0
	v_cvt_pk_f16_f32 v5, v32, v33
	global_load_lds_dwordx4 v[8:9], off
	v_cvt_pk_f16_f32 v4, v30, v31
	ds_write_b64 v100, v[4:5] offset:32768
	global_load_dwordx4 v[4:7], v201, s[80:81] nt
	s_setprio 1
	s_waitcnt lgkmcnt(1)
	v_mfma_f32_16x16x32_f16 v[30:33], v[50:53], v[218:221], v[62:65]
	v_mfma_f32_16x16x32_f16 v[70:73], v[50:53], v[222:225], v[70:73]
	v_mfma_f32_16x16x32_f16 v[104:107], v[50:53], v[226:229], v[104:107]
	v_mfma_f32_16x16x32_f16 v[108:111], v[54:57], v[218:221], v[108:111]
	v_mfma_f32_16x16x32_f16 v[112:115], v[54:57], v[222:225], v[112:115]
	v_mfma_f32_16x16x32_f16 v[116:119], v[54:57], v[226:229], v[116:119]
	v_mfma_f32_16x16x32_f16 v[234:237], v[50:53], v[230:233], v[238:241]
	v_mfma_f32_16x16x32_f16 v[238:241], v[54:57], v[230:233], v[242:245]
	s_setprio 0
	ds_read_b128 v[54:57], v129 offset:4096
	ds_read_b128 v[62:65], v129 offset:6144
	s_mov_b32 m0, s1
	v_lshl_add_u64 v[50:51], v[8:9], 0, s[58:59]
	global_load_lds_dwordx4 v[50:51], off
	v_cvt_pk_f16_f32 v29, v28, v29
	v_cvt_pk_f16_f32 v28, v26, v27
	ds_write_b64 v100, v[28:29] offset:36864
	s_add_u32 s0, s22, 0x20500
	s_addc_u32 s1, s90, 0
	global_load_dwordx4 v[50:53], v201, s[0:1] nt
	s_setprio 1
	s_waitcnt lgkmcnt(1)
	v_mfma_f32_16x16x32_f16 v[26:29], v[54:57], v[218:221], v[58:61]
	v_mfma_f32_16x16x32_f16 v[120:123], v[54:57], v[230:233], v[120:123]
	v_mfma_f32_16x16x32_f16 v[124:127], v[62:65], v[218:221], v[124:127]
	v_mfma_f32_16x16x32_f16 v[146:149], v[62:65], v[222:225], v[146:149]
	v_mfma_f32_16x16x32_f16 v[134:137], v[62:65], v[230:233], v[134:137]
	v_mfma_f32_16x16x32_f16 v[138:141], v[54:57], v[222:225], v[138:141]
	v_mfma_f32_16x16x32_f16 v[142:145], v[54:57], v[226:229], v[142:145]
	v_mfma_f32_16x16x32_f16 v[150:153], v[62:65], v[226:229], v[150:153]
	s_setprio 0
	ds_read_b128 v[58:61], v129 offset:8192
	ds_read_b128 v[62:65], v129 offset:10240
	s_mov_b32 m0, s71
	v_lshl_add_u64 v[54:55], v[8:9], 0, s[60:61]
	global_load_lds_dwordx4 v[54:55], off
	v_cvt_pk_f16_f32 v25, v24, v25
	v_cvt_pk_f16_f32 v24, v22, v23
	ds_write_b64 v100, v[24:25] offset:40960
	s_add_u32 s0, s22, 0x40500
	s_addc_u32 s1, s90, 0
	global_load_dwordx4 v[54:57], v201, s[0:1] nt
	s_setprio 1
	s_waitcnt lgkmcnt(1)
	v_mfma_f32_16x16x32_f16 v[22:25], v[58:61], v[218:221], v[246:249]
	v_mfma_f32_16x16x32_f16 v[170:173], v[58:61], v[222:225], v[170:173]
	v_mfma_f32_16x16x32_f16 v[174:177], v[58:61], v[226:229], v[174:177]
	v_mfma_f32_16x16x32_f16 v[162:165], v[58:61], v[230:233], v[162:165]
	v_mfma_f32_16x16x32_f16 v[178:181], v[62:65], v[218:221], v[178:181]
	v_mfma_f32_16x16x32_f16 v[182:185], v[62:65], v[222:225], v[182:185]
	v_mfma_f32_16x16x32_f16 v[186:189], v[62:65], v[226:229], v[186:189]
	v_mfma_f32_16x16x32_f16 v[154:157], v[62:65], v[230:233], v[154:157]
	s_setprio 0
	ds_read_b128 v[62:65], v129 offset:12288
	ds_read_b128 v[242:245], v129 offset:14336
	s_mov_b32 m0, s72
	v_lshl_add_u64 v[8:9], v[8:9], 0, s[62:63]
	global_load_lds_dwordx4 v[8:9], off
	v_cvt_pk_f16_f32 v9, v20, v21
	v_cvt_pk_f16_f32 v8, v18, v19
	ds_write_b64 v100, v[8:9] offset:45056
	s_add_u32 s0, s22, 0x60500
	s_addc_u32 s1, s90, 0
	global_load_dwordx4 v[58:61], v201, s[0:1] nt
	s_setprio 1
	s_waitcnt lgkmcnt(1)
	v_mfma_f32_16x16x32_f16 v[18:21], v[62:65], v[218:221], v[66:69]
	v_mfma_f32_16x16x32_f16 v[158:161], v[62:65], v[222:225], v[158:161]
	v_mfma_f32_16x16x32_f16 v[210:213], v[62:65], v[226:229], v[210:213]
	v_mfma_f32_16x16x32_f16 v[166:169], v[62:65], v[230:233], v[166:169]
	v_mfma_f32_16x16x32_f16 v[190:193], v[242:245], v[218:221], v[190:193]
	v_mfma_f32_16x16x32_f16 v[202:205], v[242:245], v[222:225], v[202:205]
	v_mfma_f32_16x16x32_f16 v[206:209], v[242:245], v[226:229], v[206:209]
	v_mfma_f32_16x16x32_f16 v[214:217], v[242:245], v[230:233], v[214:217]
	s_setprio 0
	ds_read_b128 v[218:221], v128
	ds_read_b128 v[222:225], v128 offset:2048
	ds_read_b128 v[226:229], v128 offset:4096
	ds_read_b128 v[230:233], v128 offset:6144
	ds_read_b128 v[66:69], v130
	ds_read_b128 v[242:245], v130 offset:2048
	v_cvt_pk_f16_f32 v9, v16, v17
	v_cvt_pk_f16_f32 v8, v14, v15
	ds_write_b64 v100, v[8:9] offset:49152
	s_add_u32 s0, s22, 0x80500
	s_addc_u32 s1, s90, 0
	global_load_dwordx4 v[62:65], v201, s[0:1] nt
	s_setprio 1
	s_waitcnt lgkmcnt(1)
	v_mfma_f32_16x16x32_f16 v[14:17], v[66:69], v[218:221], v[30:33]
	v_mfma_f32_16x16x32_f16 v[30:33], v[66:69], v[222:225], v[70:73]
	v_mfma_f32_16x16x32_f16 v[104:107], v[66:69], v[226:229], v[104:107]
	v_mfma_f32_16x16x32_f16 v[108:111], v[242:245], v[218:221], v[108:111]
	v_mfma_f32_16x16x32_f16 v[112:115], v[242:245], v[222:225], v[112:115]
	v_mfma_f32_16x16x32_f16 v[116:119], v[242:245], v[226:229], v[116:119]
	v_mfma_f32_16x16x32_f16 v[234:237], v[66:69], v[230:233], v[234:237]
	v_mfma_f32_16x16x32_f16 v[238:241], v[242:245], v[230:233], v[238:241]
	s_setprio 0
	ds_read_b128 v[70:73], v130 offset:4096
	ds_read_b128 v[242:245], v130 offset:6144
	v_cvt_pk_f16_f32 v9, v12, v13
	v_cvt_pk_f16_f32 v8, v10, v11
	ds_write_b64 v100, v[8:9] offset:53248
	s_add_u32 s0, s22, 0xa0500
	s_addc_u32 s1, s90, 0
	global_load_dwordx4 v[66:69], v201, s[0:1] nt
	s_setprio 1
	s_waitcnt lgkmcnt(1)
	v_mfma_f32_16x16x32_f16 v[26:29], v[70:73], v[218:221], v[26:29]
	v_mfma_f32_16x16x32_f16 v[120:123], v[70:73], v[230:233], v[120:123]
	v_mfma_f32_16x16x32_f16 v[124:127], v[242:245], v[218:221], v[124:127]
	v_mfma_f32_16x16x32_f16 v[146:149], v[242:245], v[222:225], v[146:149]
	v_mfma_f32_16x16x32_f16 v[134:137], v[242:245], v[230:233], v[134:137]
	v_mfma_f32_16x16x32_f16 v[138:141], v[70:73], v[222:225], v[138:141]
	v_mfma_f32_16x16x32_f16 v[142:145], v[70:73], v[226:229], v[142:145]
	v_mfma_f32_16x16x32_f16 v[150:153], v[242:245], v[226:229], v[150:153]
	s_setprio 0
	ds_read_b128 v[8:11], v130 offset:8192
	ds_read_b128 v[242:245], v130 offset:10240
	v_cvt_pk_f16_f32 v13, v36, v37
	v_cvt_pk_f16_f32 v12, v34, v35
	ds_write_b64 v100, v[12:13] offset:57344
	s_add_u32 s0, s22, 0xc0500
	s_addc_u32 s1, s90, 0
	global_load_dwordx4 v[70:73], v201, s[0:1] nt
	s_setprio 1
	s_waitcnt lgkmcnt(1)
	v_mfma_f32_16x16x32_f16 v[22:25], v[8:11], v[218:221], v[22:25]
	v_mfma_f32_16x16x32_f16 v[170:173], v[8:11], v[222:225], v[170:173]
	v_mfma_f32_16x16x32_f16 v[174:177], v[8:11], v[226:229], v[174:177]
	v_mfma_f32_16x16x32_f16 v[162:165], v[8:11], v[230:233], v[162:165]
	v_mfma_f32_16x16x32_f16 v[178:181], v[242:245], v[218:221], v[178:181]
	v_mfma_f32_16x16x32_f16 v[182:185], v[242:245], v[222:225], v[182:185]
	v_mfma_f32_16x16x32_f16 v[186:189], v[242:245], v[226:229], v[186:189]
	v_mfma_f32_16x16x32_f16 v[154:157], v[242:245], v[230:233], v[154:157]
	s_setprio 0
	ds_read_b128 v[8:11], v130 offset:12288
	ds_read_b128 v[242:245], v130 offset:14336
	v_cvt_pk_f16_f32 v13, v40, v41
	v_cvt_pk_f16_f32 v12, v38, v39
	ds_write_b64 v100, v[12:13] offset:61440
	s_add_u32 s0, s22, 0xe0500
	s_addc_u32 s1, s90, 0
	global_load_dwordx4 v[36:39], v201, s[0:1] nt
	s_setprio 1
	s_waitcnt lgkmcnt(1)
	v_mfma_f32_16x16x32_f16 v[246:249], v[8:11], v[218:221], v[18:21]
	v_mfma_f32_16x16x32_f16 v[158:161], v[8:11], v[222:225], v[158:161]
	v_mfma_f32_16x16x32_f16 v[210:213], v[8:11], v[226:229], v[210:213]
	v_mfma_f32_16x16x32_f16 v[166:169], v[8:11], v[230:233], v[166:169]
	v_mfma_f32_16x16x32_f16 v[190:193], v[242:245], v[218:221], v[190:193]
	v_mfma_f32_16x16x32_f16 v[202:205], v[242:245], v[222:225], v[202:205]
	v_mfma_f32_16x16x32_f16 v[206:209], v[242:245], v[226:229], v[206:209]
	v_mfma_f32_16x16x32_f16 v[214:217], v[242:245], v[230:233], v[214:217]
	s_setprio 0
	s_waitcnt vmcnt(5)
	s_waitcnt lgkmcnt(0)
	s_barrier
	ds_read_b128 v[218:221], v131 offset:32768
	ds_read_b128 v[222:225], v131 offset:34816
	ds_read_b128 v[226:229], v131 offset:36864
	ds_read_b128 v[230:233], v131 offset:38912
	ds_read_b128 v[8:11], v129 offset:32768
	ds_read_b128 v[18:21], v129 offset:34816
	s_add_u32 s0, s22, 0x600
	s_addc_u32 s1, s90, 0
	v_lshl_add_u64 v[34:35], s[34:35], 0, v[196:197]
	s_mov_b32 m0, s70
	v_cvt_pk_f16_f32 v3, v2, v3
	global_load_lds_dwordx4 v[34:35], off
	v_cvt_pk_f16_f32 v2, v0, v1
	ds_write_b64 v100, v[2:3]
	global_load_dwordx4 v[0:3], v201, s[0:1] nt
	s_setprio 1
	s_waitcnt lgkmcnt(1)
	v_mfma_f32_16x16x32_f16 v[30:33], v[8:11], v[222:225], v[30:33]
	v_mfma_f32_16x16x32_f16 v[104:107], v[8:11], v[226:229], v[104:107]
	v_mfma_f32_16x16x32_f16 v[108:111], v[18:21], v[218:221], v[108:111]
	v_mfma_f32_16x16x32_f16 v[112:115], v[18:21], v[222:225], v[112:115]
	v_mfma_f32_16x16x32_f16 v[116:119], v[18:21], v[226:229], v[116:119]
	v_mfma_f32_16x16x32_f16 v[242:245], v[8:11], v[218:221], v[14:17]
	v_mfma_f32_16x16x32_f16 v[234:237], v[8:11], v[230:233], v[234:237]
	v_mfma_f32_16x16x32_f16 v[238:241], v[18:21], v[230:233], v[238:241]
	s_setprio 0
	ds_read_b128 v[12:15], v129 offset:36864
	ds_read_b128 v[16:19], v129 offset:38912
	s_mov_b32 m0, s73
	v_lshl_add_u64 v[8:9], v[34:35], 0, s[58:59]
	global_load_lds_dwordx4 v[8:9], off
	v_cvt_pk_f16_f32 v9, v44, v45
	v_cvt_pk_f16_f32 v8, v42, v43
	ds_write_b64 v100, v[8:9] offset:4096
	s_add_u32 s0, s22, 0x20600
	s_addc_u32 s1, s90, 0
	global_load_dwordx4 v[8:11], v201, s[0:1] nt
	s_setprio 1
	s_waitcnt lgkmcnt(1)
	v_mfma_f32_16x16x32_f16 v[40:43], v[12:15], v[218:221], v[26:29]
	v_mfma_f32_16x16x32_f16 v[120:123], v[12:15], v[230:233], v[120:123]
	v_mfma_f32_16x16x32_f16 v[124:127], v[16:19], v[218:221], v[124:127]
	v_mfma_f32_16x16x32_f16 v[146:149], v[16:19], v[222:225], v[146:149]
	v_mfma_f32_16x16x32_f16 v[134:137], v[16:19], v[230:233], v[134:137]
	v_mfma_f32_16x16x32_f16 v[138:141], v[12:15], v[222:225], v[138:141]
	v_mfma_f32_16x16x32_f16 v[142:145], v[12:15], v[226:229], v[142:145]
	v_mfma_f32_16x16x32_f16 v[150:153], v[16:19], v[226:229], v[150:153]
	s_setprio 0
	ds_read_b128 v[16:19], v129 offset:40960
	ds_read_b128 v[26:29], v129 offset:43008
	s_mov_b32 m0, s91
	v_lshl_add_u64 v[12:13], v[34:35], 0, s[60:61]
	global_load_lds_dwordx4 v[12:13], off
	v_cvt_pk_f16_f32 v13, v48, v49
	v_cvt_pk_f16_f32 v12, v46, v47
	ds_write_b64 v100, v[12:13] offset:8192
	s_add_u32 s0, s22, 0x40600
	s_addc_u32 s1, s90, 0
	global_load_dwordx4 v[12:15], v201, s[0:1] nt
	s_setprio 1
	s_waitcnt lgkmcnt(1)
	v_mfma_f32_16x16x32_f16 v[44:47], v[16:19], v[218:221], v[22:25]
	v_mfma_f32_16x16x32_f16 v[170:173], v[16:19], v[222:225], v[170:173]
	v_mfma_f32_16x16x32_f16 v[174:177], v[16:19], v[226:229], v[174:177]
	v_mfma_f32_16x16x32_f16 v[162:165], v[16:19], v[230:233], v[162:165]
	v_mfma_f32_16x16x32_f16 v[178:181], v[26:29], v[218:221], v[178:181]
	v_mfma_f32_16x16x32_f16 v[182:185], v[26:29], v[222:225], v[182:185]
	v_mfma_f32_16x16x32_f16 v[186:189], v[26:29], v[226:229], v[186:189]
	v_mfma_f32_16x16x32_f16 v[154:157], v[26:29], v[230:233], v[154:157]
	s_setprio 0
	ds_read_b128 v[20:23], v129 offset:45056
	ds_read_b128 v[24:27], v129 offset:47104
	s_mov_b32 m0, s92
	v_lshl_add_u64 v[16:17], v[34:35], 0, s[62:63]
	global_load_lds_dwordx4 v[16:17], off
	v_cvt_pk_f16_f32 v17, v76, v77
	v_cvt_pk_f16_f32 v16, v74, v75
	ds_write_b64 v100, v[16:17] offset:12288
	s_add_u32 s0, s22, 0x60600
	s_addc_u32 s1, s90, 0
	global_load_dwordx4 v[16:19], v201, s[0:1] nt
	s_setprio 1
	s_waitcnt lgkmcnt(1)
	v_mfma_f32_16x16x32_f16 v[74:77], v[20:23], v[218:221], v[246:249]
	v_mfma_f32_16x16x32_f16 v[158:161], v[20:23], v[222:225], v[158:161]
	v_mfma_f32_16x16x32_f16 v[210:213], v[20:23], v[226:229], v[210:213]
	v_mfma_f32_16x16x32_f16 v[166:169], v[20:23], v[230:233], v[166:169]
	v_mfma_f32_16x16x32_f16 v[190:193], v[24:27], v[218:221], v[190:193]
	v_mfma_f32_16x16x32_f16 v[202:205], v[24:27], v[222:225], v[202:205]
	v_mfma_f32_16x16x32_f16 v[206:209], v[24:27], v[226:229], v[206:209]
	v_mfma_f32_16x16x32_f16 v[214:217], v[24:27], v[230:233], v[214:217]
	s_setprio 0
	ds_read_b128 v[218:221], v128 offset:32768
	ds_read_b128 v[222:225], v128 offset:34816
	ds_read_b128 v[226:229], v128 offset:36864
	ds_read_b128 v[230:233], v128 offset:38912
	ds_read_b128 v[24:27], v130 offset:32768
	ds_read_b128 v[246:249], v130 offset:34816
	v_cvt_pk_f16_f32 v21, v80, v81
	v_cvt_pk_f16_f32 v20, v78, v79
	ds_write_b64 v100, v[20:21] offset:16384
	s_add_u32 s0, s22, 0x80600
	s_addc_u32 s1, s90, 0
	global_load_dwordx4 v[20:23], v201, s[0:1] nt
	s_setprio 1
	s_waitcnt lgkmcnt(1)
	v_mfma_f32_16x16x32_f16 v[78:81], v[24:27], v[218:221], v[242:245]
	v_mfma_f32_16x16x32_f16 v[104:107], v[24:27], v[226:229], v[104:107]
	v_mfma_f32_16x16x32_f16 v[108:111], v[246:249], v[218:221], v[108:111]
	v_mfma_f32_16x16x32_f16 v[112:115], v[246:249], v[222:225], v[112:115]
	v_mfma_f32_16x16x32_f16 v[116:119], v[246:249], v[226:229], v[116:119]
	v_mfma_f32_16x16x32_f16 v[242:245], v[24:27], v[222:225], v[30:33]
	v_mfma_f32_16x16x32_f16 v[234:237], v[24:27], v[230:233], v[234:237]
	v_mfma_f32_16x16x32_f16 v[238:241], v[246:249], v[230:233], v[238:241]
	s_setprio 0
	ds_read_b128 v[28:31], v130 offset:36864
	ds_read_b128 v[32:35], v130 offset:38912
	v_cvt_pk_f16_f32 v25, v84, v85
	v_cvt_pk_f16_f32 v24, v82, v83
	ds_write_b64 v100, v[24:25] offset:20480
	s_add_u32 s0, s22, 0xa0600
	s_addc_u32 s1, s90, 0
	global_load_dwordx4 v[24:27], v201, s[0:1] nt
	s_setprio 1
	s_waitcnt lgkmcnt(1)
	v_mfma_f32_16x16x32_f16 v[82:85], v[28:31], v[218:221], v[40:43]
	v_mfma_f32_16x16x32_f16 v[120:123], v[28:31], v[230:233], v[120:123]
	v_mfma_f32_16x16x32_f16 v[124:127], v[32:35], v[218:221], v[124:127]
	v_mfma_f32_16x16x32_f16 v[146:149], v[32:35], v[222:225], v[146:149]
	v_mfma_f32_16x16x32_f16 v[134:137], v[32:35], v[230:233], v[134:137]
	v_mfma_f32_16x16x32_f16 v[138:141], v[28:31], v[222:225], v[138:141]
	v_mfma_f32_16x16x32_f16 v[142:145], v[28:31], v[226:229], v[142:145]
	v_mfma_f32_16x16x32_f16 v[150:153], v[32:35], v[226:229], v[150:153]
	s_setprio 0
	ds_read_b128 v[32:35], v130 offset:40960
	ds_read_b128 v[40:43], v130 offset:43008
	v_cvt_pk_f16_f32 v29, v88, v89
	v_cvt_pk_f16_f32 v28, v86, v87
	ds_write_b64 v100, v[28:29] offset:24576
	s_add_u32 s0, s22, 0xc0600
	s_addc_u32 s1, s90, 0
	global_load_dwordx4 v[28:31], v201, s[0:1] nt
	s_setprio 1
	s_waitcnt lgkmcnt(1)
	v_mfma_f32_16x16x32_f16 v[86:89], v[32:35], v[218:221], v[44:47]
	v_mfma_f32_16x16x32_f16 v[170:173], v[32:35], v[222:225], v[170:173]
	v_mfma_f32_16x16x32_f16 v[174:177], v[32:35], v[226:229], v[174:177]
	v_mfma_f32_16x16x32_f16 v[162:165], v[32:35], v[230:233], v[162:165]
	v_mfma_f32_16x16x32_f16 v[178:181], v[40:43], v[218:221], v[178:181]
	v_mfma_f32_16x16x32_f16 v[182:185], v[40:43], v[222:225], v[182:185]
	v_mfma_f32_16x16x32_f16 v[186:189], v[40:43], v[226:229], v[186:189]
	v_mfma_f32_16x16x32_f16 v[154:157], v[40:43], v[230:233], v[154:157]
	s_setprio 0
	ds_read_b128 v[40:43], v130 offset:45056
	ds_read_b128 v[44:47], v130 offset:47104
	v_cvt_pk_f16_f32 v33, v92, v93
	v_cvt_pk_f16_f32 v32, v90, v91
	ds_write_b64 v100, v[32:33] offset:28672
	s_add_u32 s0, s22, 0xe0600
	s_addc_u32 s1, s90, 0
	global_load_dwordx4 v[32:35], v201, s[0:1] nt
	s_setprio 1
	s_waitcnt lgkmcnt(1)
	v_mfma_f32_16x16x32_f16 v[74:77], v[40:43], v[218:221], v[74:77]
	v_mfma_f32_16x16x32_f16 v[90:93], v[40:43], v[222:225], v[158:161]
	v_mfma_f32_16x16x32_f16 v[158:161], v[40:43], v[226:229], v[210:213]
	v_mfma_f32_16x16x32_f16 v[166:169], v[40:43], v[230:233], v[166:169]
	v_mfma_f32_16x16x32_f16 v[190:193], v[44:47], v[218:221], v[190:193]
	v_mfma_f32_16x16x32_f16 v[202:205], v[44:47], v[222:225], v[202:205]
	v_mfma_f32_16x16x32_f16 v[206:209], v[44:47], v[226:229], v[206:209]
	v_mfma_f32_16x16x32_f16 v[210:213], v[44:47], v[230:233], v[214:217]
	s_setprio 0
	s_waitcnt vmcnt(5)
	s_waitcnt lgkmcnt(0)
	s_barrier
	s_nop 0
	ds_read_b128 v[214:217], v131
	ds_read_b128 v[218:221], v131 offset:2048
	ds_read_b128 v[222:225], v131 offset:4096
	ds_read_b128 v[226:229], v131 offset:6144
	ds_read_b128 v[40:43], v129
	ds_read_b128 v[44:47], v129 offset:2048
	s_add_u32 s70, s22, 0x700
	s_addc_u32 s71, s90, 0
	v_lshl_add_u64 v[198:199], s[36:37], 0, v[196:197]
	v_readfirstlane_b32 s0, v95
	s_mov_b32 m0, s0
	v_cvt_pk_f16_f32 v7, v6, v7
	global_load_lds_dwordx4 v[198:199], off
	v_cvt_pk_f16_f32 v6, v4, v5
	ds_write_b64 v100, v[6:7] offset:32768
	global_load_dwordx4 v[4:7], v201, s[70:71] nt
	s_setprio 1
	s_waitcnt lgkmcnt(1)
	v_mfma_f32_16x16x32_f16 v[78:81], v[40:43], v[214:217], v[78:81]
	v_mfma_f32_16x16x32_f16 v[104:107], v[40:43], v[222:225], v[104:107]
	v_mfma_f32_16x16x32_f16 v[108:111], v[44:47], v[214:217], v[108:111]
	v_mfma_f32_16x16x32_f16 v[112:115], v[44:47], v[218:221], v[112:115]
	v_mfma_f32_16x16x32_f16 v[116:119], v[44:47], v[222:225], v[116:119]
	v_mfma_f32_16x16x32_f16 v[230:233], v[40:43], v[218:221], v[242:245]
	v_mfma_f32_16x16x32_f16 v[234:237], v[40:43], v[226:229], v[234:237]
	v_mfma_f32_16x16x32_f16 v[238:241], v[44:47], v[226:229], v[238:241]
	s_setprio 0
	ds_read_b128 v[44:47], v129 offset:4096
	ds_read_b128 v[242:245], v129 offset:6144
	v_readfirstlane_b32 s72, v96
	v_lshl_add_u64 v[40:41], v[198:199], 0, s[58:59]
	s_mov_b32 m0, s72
	s_nop 0
	global_load_lds_dwordx4 v[40:41], off
	v_cvt_pk_f16_f32 v41, v52, v53
	v_cvt_pk_f16_f32 v40, v50, v51
	ds_write_b64 v100, v[40:41] offset:36864
	s_add_u32 s70, s22, 0x20700
	s_addc_u32 s71, s90, 0
	global_load_dwordx4 v[40:43], v201, s[70:71] nt
	s_setprio 1
	s_waitcnt lgkmcnt(1)
	v_mfma_f32_16x16x32_f16 v[82:85], v[44:47], v[214:217], v[82:85]
	v_mfma_f32_16x16x32_f16 v[120:123], v[44:47], v[226:229], v[120:123]
	v_mfma_f32_16x16x32_f16 v[124:127], v[242:245], v[214:217], v[124:127]
	v_mfma_f32_16x16x32_f16 v[146:149], v[242:245], v[218:221], v[146:149]
	v_mfma_f32_16x16x32_f16 v[134:137], v[242:245], v[226:229], v[134:137]
	v_mfma_f32_16x16x32_f16 v[138:141], v[44:47], v[218:221], v[138:141]
	v_mfma_f32_16x16x32_f16 v[142:145], v[44:47], v[222:225], v[142:145]
	v_mfma_f32_16x16x32_f16 v[150:153], v[242:245], v[222:225], v[150:153]
	s_setprio 0
	ds_read_b128 v[48:51], v129 offset:8192
	ds_read_b128 v[242:245], v129 offset:10240
	v_readfirstlane_b32 s71, v97
	v_lshl_add_u64 v[44:45], v[198:199], 0, s[60:61]
	s_mov_b32 m0, s71
	s_nop 0
	global_load_lds_dwordx4 v[44:45], off
	v_cvt_pk_f16_f32 v45, v56, v57
	v_cvt_pk_f16_f32 v44, v54, v55
	ds_write_b64 v100, v[44:45] offset:40960
	s_add_u32 s80, s22, 0x40700
	s_addc_u32 s81, s90, 0
	global_load_dwordx4 v[44:47], v201, s[80:81] nt
	s_setprio 1
	s_waitcnt lgkmcnt(1)
	v_mfma_f32_16x16x32_f16 v[86:89], v[48:51], v[214:217], v[86:89]
	v_mfma_f32_16x16x32_f16 v[170:173], v[48:51], v[218:221], v[170:173]
	v_mfma_f32_16x16x32_f16 v[174:177], v[48:51], v[222:225], v[174:177]
	v_mfma_f32_16x16x32_f16 v[162:165], v[48:51], v[226:229], v[162:165]
	v_mfma_f32_16x16x32_f16 v[178:181], v[242:245], v[214:217], v[178:181]
	v_mfma_f32_16x16x32_f16 v[182:185], v[242:245], v[218:221], v[182:185]
	v_mfma_f32_16x16x32_f16 v[186:189], v[242:245], v[222:225], v[186:189]
	v_mfma_f32_16x16x32_f16 v[154:157], v[242:245], v[226:229], v[154:157]
	s_setprio 0
	ds_read_b128 v[52:55], v129 offset:12288
	ds_read_b128 v[242:245], v129 offset:14336
	v_readfirstlane_b32 s70, v98
	v_lshl_add_u64 v[48:49], v[198:199], 0, s[62:63]
	s_mov_b32 m0, s70
	s_nop 0
	global_load_lds_dwordx4 v[48:49], off
	v_cvt_pk_f16_f32 v49, v60, v61
	v_cvt_pk_f16_f32 v48, v58, v59
	ds_write_b64 v100, v[48:49] offset:45056
	s_add_u32 s80, s22, 0x60700
	s_addc_u32 s81, s90, 0
	global_load_dwordx4 v[48:51], v201, s[80:81] nt
	s_setprio 1
	s_waitcnt lgkmcnt(1)
	v_mfma_f32_16x16x32_f16 v[74:77], v[52:55], v[214:217], v[74:77]
	v_mfma_f32_16x16x32_f16 v[90:93], v[52:55], v[218:221], v[90:93]
	v_mfma_f32_16x16x32_f16 v[158:161], v[52:55], v[222:225], v[158:161]
	v_mfma_f32_16x16x32_f16 v[166:169], v[52:55], v[226:229], v[166:169]
	v_mfma_f32_16x16x32_f16 v[190:193], v[242:245], v[214:217], v[190:193]
	v_mfma_f32_16x16x32_f16 v[202:205], v[242:245], v[218:221], v[202:205]
	v_mfma_f32_16x16x32_f16 v[206:209], v[242:245], v[222:225], v[206:209]
	v_mfma_f32_16x16x32_f16 v[210:213], v[242:245], v[226:229], v[210:213]
	s_setprio 0
	ds_read_b128 v[214:217], v128
	ds_read_b128 v[218:221], v128 offset:2048
	ds_read_b128 v[222:225], v128 offset:4096
	ds_read_b128 v[226:229], v128 offset:6144
	ds_read_b128 v[56:59], v130
	ds_read_b128 v[242:245], v130 offset:2048
	v_cvt_pk_f16_f32 v53, v64, v65
	v_cvt_pk_f16_f32 v52, v62, v63
	ds_write_b64 v100, v[52:53] offset:49152
	s_add_u32 s80, s22, 0x80700
	s_addc_u32 s81, s90, 0
	global_load_dwordx4 v[52:55], v201, s[80:81] nt
	s_setprio 1
	s_waitcnt lgkmcnt(1)
	v_mfma_f32_16x16x32_f16 v[78:81], v[56:59], v[214:217], v[78:81]
	v_mfma_f32_16x16x32_f16 v[104:107], v[56:59], v[222:225], v[104:107]
	v_mfma_f32_16x16x32_f16 v[108:111], v[242:245], v[214:217], v[108:111]
	v_mfma_f32_16x16x32_f16 v[112:115], v[242:245], v[218:221], v[112:115]
	v_mfma_f32_16x16x32_f16 v[116:119], v[242:245], v[222:225], v[116:119]
	v_mfma_f32_16x16x32_f16 v[230:233], v[56:59], v[218:221], v[230:233]
	v_mfma_f32_16x16x32_f16 v[234:237], v[56:59], v[226:229], v[234:237]
	v_mfma_f32_16x16x32_f16 v[238:241], v[242:245], v[226:229], v[238:241]
	s_setprio 0
	ds_read_b128 v[60:63], v130 offset:4096
	ds_read_b128 v[242:245], v130 offset:6144
	v_cvt_pk_f16_f32 v57, v68, v69
	v_cvt_pk_f16_f32 v56, v66, v67
	ds_write_b64 v100, v[56:57] offset:53248
	s_add_u32 s80, s22, 0xa0700
	s_addc_u32 s81, s90, 0
	global_load_dwordx4 v[56:59], v201, s[80:81] nt
	s_setprio 1
	s_waitcnt lgkmcnt(1)
	v_mfma_f32_16x16x32_f16 v[82:85], v[60:63], v[214:217], v[82:85]
	v_mfma_f32_16x16x32_f16 v[120:123], v[60:63], v[226:229], v[120:123]
	v_mfma_f32_16x16x32_f16 v[124:127], v[242:245], v[214:217], v[124:127]
	v_mfma_f32_16x16x32_f16 v[146:149], v[242:245], v[218:221], v[146:149]
	v_mfma_f32_16x16x32_f16 v[134:137], v[242:245], v[226:229], v[134:137]
	v_mfma_f32_16x16x32_f16 v[138:141], v[60:63], v[218:221], v[138:141]
	v_mfma_f32_16x16x32_f16 v[142:145], v[60:63], v[222:225], v[142:145]
	v_mfma_f32_16x16x32_f16 v[150:153], v[242:245], v[222:225], v[150:153]
	s_setprio 0
	ds_read_b128 v[64:67], v130 offset:8192
	ds_read_b128 v[242:245], v130 offset:10240
	v_cvt_pk_f16_f32 v61, v72, v73
	v_cvt_pk_f16_f32 v60, v70, v71
	ds_write_b64 v100, v[60:61] offset:57344
	s_add_u32 s80, s22, 0xc0700
	s_addc_u32 s81, s90, 0
	global_load_dwordx4 v[60:63], v201, s[80:81] nt
	s_setprio 1
	s_waitcnt lgkmcnt(1)
	v_mfma_f32_16x16x32_f16 v[86:89], v[64:67], v[214:217], v[86:89]
	v_mfma_f32_16x16x32_f16 v[170:173], v[64:67], v[218:221], v[170:173]
	v_mfma_f32_16x16x32_f16 v[174:177], v[64:67], v[222:225], v[174:177]
	v_mfma_f32_16x16x32_f16 v[162:165], v[64:67], v[226:229], v[162:165]
	v_mfma_f32_16x16x32_f16 v[178:181], v[242:245], v[214:217], v[178:181]
	v_mfma_f32_16x16x32_f16 v[182:185], v[242:245], v[218:221], v[182:185]
	v_mfma_f32_16x16x32_f16 v[186:189], v[242:245], v[222:225], v[186:189]
	v_mfma_f32_16x16x32_f16 v[154:157], v[242:245], v[226:229], v[154:157]
	s_setprio 0
	ds_read_b128 v[64:67], v130 offset:12288
	ds_read_b128 v[68:71], v130 offset:14336
	v_cvt_pk_f16_f32 v39, v38, v39
	v_cvt_pk_f16_f32 v38, v36, v37
	ds_write_b64 v100, v[38:39] offset:61440
	s_add_u32 s80, s22, 0xe0700
	s_addc_u32 s81, s90, 0
	global_load_dwordx4 v[36:39], v201, s[80:81] nt
	s_setprio 1
	s_waitcnt lgkmcnt(1)
	v_mfma_f32_16x16x32_f16 v[90:93], v[64:67], v[218:221], v[90:93]
	v_mfma_f32_16x16x32_f16 v[242:245], v[64:67], v[214:217], v[74:77]
	v_mfma_f32_16x16x32_f16 v[158:161], v[64:67], v[222:225], v[158:161]
	v_mfma_f32_16x16x32_f16 v[166:169], v[64:67], v[226:229], v[166:169]
	v_mfma_f32_16x16x32_f16 v[190:193], v[68:71], v[214:217], v[190:193]
	v_mfma_f32_16x16x32_f16 v[202:205], v[68:71], v[218:221], v[202:205]
	v_mfma_f32_16x16x32_f16 v[206:209], v[68:71], v[222:225], v[206:209]
	v_mfma_f32_16x16x32_f16 v[210:213], v[68:71], v[226:229], v[210:213]
	s_setprio 0
	s_waitcnt vmcnt(5)
	s_waitcnt lgkmcnt(0)
	s_barrier
	ds_read_b128 v[214:217], v131 offset:32768
	ds_read_b128 v[218:221], v131 offset:34816
	ds_read_b128 v[222:225], v131 offset:36864
	ds_read_b128 v[226:229], v131 offset:38912
	ds_read_b128 v[64:67], v129 offset:32768
	ds_read_b128 v[68:71], v129 offset:34816
	s_add_u32 s80, s22, 0x800
	s_addc_u32 s81, s90, 0
	v_lshl_add_u64 v[198:199], s[38:39], 0, v[196:197]
	v_readfirstlane_b32 s1, v94
	s_mov_b32 m0, s1
	v_cvt_pk_f16_f32 v3, v2, v3
	global_load_lds_dwordx4 v[198:199], off
	v_cvt_pk_f16_f32 v2, v0, v1
	ds_write_b64 v100, v[2:3]
	global_load_dwordx4 v[0:3], v201, s[80:81] nt
	s_setprio 1
	s_waitcnt lgkmcnt(1)
	v_mfma_f32_16x16x32_f16 v[104:107], v[64:67], v[222:225], v[104:107]
	v_mfma_f32_16x16x32_f16 v[108:111], v[68:71], v[214:217], v[108:111]
	v_mfma_f32_16x16x32_f16 v[112:115], v[68:71], v[218:221], v[112:115]
	v_mfma_f32_16x16x32_f16 v[116:119], v[68:71], v[222:225], v[116:119]
	v_mfma_f32_16x16x32_f16 v[246:249], v[64:67], v[214:217], v[78:81]
	v_mfma_f32_16x16x32_f16 v[230:233], v[64:67], v[218:221], v[230:233]
	v_mfma_f32_16x16x32_f16 v[234:237], v[64:67], v[226:229], v[234:237]
	v_mfma_f32_16x16x32_f16 v[238:241], v[68:71], v[226:229], v[238:241]
	s_setprio 0
	ds_read_b128 v[68:71], v129 offset:36864
	ds_read_b128 v[72:75], v129 offset:38912
	v_readfirstlane_b32 s92, v99
	v_lshl_add_u64 v[64:65], v[198:199], 0, s[58:59]
	s_mov_b32 m0, s92
	v_cvt_pk_f16_f32 v11, v10, v11
	global_load_lds_dwordx4 v[64:65], off
	v_cvt_pk_f16_f32 v10, v8, v9
	ds_write_b64 v100, v[10:11] offset:4096
	s_add_u32 s80, s22, 0x20800
	s_addc_u32 s81, s90, 0
	global_load_dwordx4 v[64:67], v201, s[80:81] nt
	s_setprio 1
	s_waitcnt lgkmcnt(1)
	v_mfma_f32_16x16x32_f16 v[8:11], v[68:71], v[214:217], v[82:85]
	v_mfma_f32_16x16x32_f16 v[120:123], v[68:71], v[226:229], v[120:123]
	v_mfma_f32_16x16x32_f16 v[124:127], v[72:75], v[214:217], v[124:127]
	v_mfma_f32_16x16x32_f16 v[146:149], v[72:75], v[218:221], v[146:149]
	v_mfma_f32_16x16x32_f16 v[134:137], v[72:75], v[226:229], v[134:137]
	v_mfma_f32_16x16x32_f16 v[138:141], v[68:71], v[218:221], v[138:141]
	v_mfma_f32_16x16x32_f16 v[142:145], v[68:71], v[222:225], v[142:145]
	v_mfma_f32_16x16x32_f16 v[150:153], v[72:75], v[222:225], v[150:153]
	s_setprio 0
	ds_read_b128 v[72:75], v129 offset:40960
	ds_read_b128 v[76:79], v129 offset:43008
	v_readfirstlane_b32 s91, v101
	v_lshl_add_u64 v[68:69], v[198:199], 0, s[60:61]
	s_mov_b32 m0, s91
	v_cvt_pk_f16_f32 v15, v14, v15
	global_load_lds_dwordx4 v[68:69], off
	v_cvt_pk_f16_f32 v14, v12, v13
	ds_write_b64 v100, v[14:15] offset:8192
	s_add_u32 s80, s22, 0x40800
	s_addc_u32 s81, s90, 0
	global_load_dwordx4 v[68:71], v201, s[80:81] nt
	s_setprio 1
	s_waitcnt lgkmcnt(1)
	v_mfma_f32_16x16x32_f16 v[12:15], v[72:75], v[214:217], v[86:89]
	v_mfma_f32_16x16x32_f16 v[170:173], v[72:75], v[218:221], v[170:173]
	v_mfma_f32_16x16x32_f16 v[174:177], v[72:75], v[222:225], v[174:177]
	v_mfma_f32_16x16x32_f16 v[162:165], v[72:75], v[226:229], v[162:165]
	v_mfma_f32_16x16x32_f16 v[178:181], v[76:79], v[214:217], v[178:181]
	v_mfma_f32_16x16x32_f16 v[182:185], v[76:79], v[218:221], v[182:185]
	v_mfma_f32_16x16x32_f16 v[186:189], v[76:79], v[222:225], v[186:189]
	v_mfma_f32_16x16x32_f16 v[154:157], v[76:79], v[226:229], v[154:157]
	s_setprio 0
	ds_read_b128 v[76:79], v129 offset:45056
	ds_read_b128 v[80:83], v129 offset:47104
	v_readfirstlane_b32 s73, v102
	v_lshl_add_u64 v[72:73], v[198:199], 0, s[62:63]
	s_mov_b32 m0, s73
	v_cvt_pk_f16_f32 v19, v18, v19
	global_load_lds_dwordx4 v[72:73], off
	v_cvt_pk_f16_f32 v18, v16, v17
	ds_write_b64 v100, v[18:19] offset:12288
	s_add_u32 s80, s22, 0x60800
	s_addc_u32 s81, s90, 0
	global_load_dwordx4 v[72:75], v201, s[80:81] nt
	s_setprio 1
	s_waitcnt lgkmcnt(1)
	v_mfma_f32_16x16x32_f16 v[16:19], v[76:79], v[214:217], v[242:245]
	v_mfma_f32_16x16x32_f16 v[242:245], v[76:79], v[218:221], v[90:93]
	v_mfma_f32_16x16x32_f16 v[158:161], v[76:79], v[222:225], v[158:161]
	v_mfma_f32_16x16x32_f16 v[166:169], v[76:79], v[226:229], v[166:169]
	v_mfma_f32_16x16x32_f16 v[190:193], v[80:83], v[214:217], v[190:193]
	v_mfma_f32_16x16x32_f16 v[202:205], v[80:83], v[218:221], v[202:205]
	v_mfma_f32_16x16x32_f16 v[206:209], v[80:83], v[222:225], v[206:209]
	v_mfma_f32_16x16x32_f16 v[210:213], v[80:83], v[226:229], v[210:213]
	s_setprio 0
	ds_read_b128 v[214:217], v128 offset:32768
	ds_read_b128 v[218:221], v128 offset:34816
	ds_read_b128 v[222:225], v128 offset:36864
	ds_read_b128 v[226:229], v128 offset:38912
	ds_read_b128 v[80:83], v130 offset:32768
	ds_read_b128 v[84:87], v130 offset:34816
	v_cvt_pk_f16_f32 v23, v22, v23
	v_cvt_pk_f16_f32 v22, v20, v21
	ds_write_b64 v100, v[22:23] offset:16384
	s_add_u32 s80, s22, 0x80800
	s_addc_u32 s81, s90, 0
	global_load_dwordx4 v[76:79], v201, s[80:81] nt
	s_setprio 1
	s_waitcnt lgkmcnt(1)
	v_mfma_f32_16x16x32_f16 v[20:23], v[80:83], v[214:217], v[246:249]
	v_mfma_f32_16x16x32_f16 v[104:107], v[80:83], v[222:225], v[104:107]
	v_mfma_f32_16x16x32_f16 v[108:111], v[84:87], v[214:217], v[108:111]
	v_mfma_f32_16x16x32_f16 v[112:115], v[84:87], v[218:221], v[112:115]
	v_mfma_f32_16x16x32_f16 v[116:119], v[84:87], v[222:225], v[116:119]
	v_mfma_f32_16x16x32_f16 v[230:233], v[80:83], v[218:221], v[230:233]
	v_mfma_f32_16x16x32_f16 v[234:237], v[80:83], v[226:229], v[234:237]
	v_mfma_f32_16x16x32_f16 v[238:241], v[84:87], v[226:229], v[238:241]
	s_setprio 0
	ds_read_b128 v[84:87], v130 offset:36864
	ds_read_b128 v[88:91], v130 offset:38912
	v_cvt_pk_f16_f32 v27, v26, v27
	v_cvt_pk_f16_f32 v26, v24, v25
	ds_write_b64 v100, v[26:27] offset:20480
	s_add_u32 s80, s22, 0xa0800
	s_addc_u32 s81, s90, 0
	global_load_dwordx4 v[80:83], v201, s[80:81] nt
	s_setprio 1
	s_waitcnt lgkmcnt(1)
	v_mfma_f32_16x16x32_f16 v[24:27], v[84:87], v[214:217], v[8:11]
	v_mfma_f32_16x16x32_f16 v[120:123], v[84:87], v[226:229], v[120:123]
	v_mfma_f32_16x16x32_f16 v[124:127], v[88:91], v[214:217], v[124:127]
	v_mfma_f32_16x16x32_f16 v[146:149], v[88:91], v[218:221], v[146:149]
	v_mfma_f32_16x16x32_f16 v[134:137], v[88:91], v[226:229], v[134:137]
	v_mfma_f32_16x16x32_f16 v[138:141], v[84:87], v[218:221], v[138:141]
	v_mfma_f32_16x16x32_f16 v[142:145], v[84:87], v[222:225], v[142:145]
	v_mfma_f32_16x16x32_f16 v[150:153], v[88:91], v[222:225], v[150:153]
	s_setprio 0
	ds_read_b128 v[8:11], v130 offset:40960
	ds_read_b128 v[88:91], v130 offset:43008
	v_cvt_pk_f16_f32 v31, v30, v31
	v_cvt_pk_f16_f32 v30, v28, v29
	ds_write_b64 v100, v[30:31] offset:24576
	s_add_u32 s80, s22, 0xc0800
	s_addc_u32 s81, s90, 0
	global_load_dwordx4 v[84:87], v201, s[80:81] nt
	s_setprio 1
	s_waitcnt lgkmcnt(1)
	v_mfma_f32_16x16x32_f16 v[12:15], v[8:11], v[214:217], v[12:15]
	v_mfma_f32_16x16x32_f16 v[28:31], v[8:11], v[218:221], v[170:173]
	v_mfma_f32_16x16x32_f16 v[170:173], v[8:11], v[222:225], v[174:177]
	v_mfma_f32_16x16x32_f16 v[162:165], v[8:11], v[226:229], v[162:165]
	v_mfma_f32_16x16x32_f16 v[174:177], v[88:91], v[214:217], v[178:181]
	v_mfma_f32_16x16x32_f16 v[178:181], v[88:91], v[218:221], v[182:185]
	v_mfma_f32_16x16x32_f16 v[182:185], v[88:91], v[222:225], v[186:189]
	v_mfma_f32_16x16x32_f16 v[154:157], v[88:91], v[226:229], v[154:157]
	s_setprio 0
	ds_read_b128 v[8:11], v130 offset:45056
	ds_read_b128 v[186:189], v130 offset:47104
	v_cvt_pk_f16_f32 v35, v34, v35
	v_cvt_pk_f16_f32 v34, v32, v33
	ds_write_b64 v100, v[34:35] offset:28672
	s_add_u32 s80, s22, 0xe0800
	s_addc_u32 s81, s90, 0
	global_load_dwordx4 v[88:91], v201, s[80:81] nt
	s_setprio 1
	s_waitcnt lgkmcnt(1)
	v_mfma_f32_16x16x32_f16 v[16:19], v[8:11], v[214:217], v[16:19]
	v_mfma_f32_16x16x32_f16 v[32:35], v[8:11], v[218:221], v[242:245]
	v_mfma_f32_16x16x32_f16 v[158:161], v[8:11], v[222:225], v[158:161]
	v_mfma_f32_16x16x32_f16 v[166:169], v[8:11], v[226:229], v[166:169]
	v_mfma_f32_16x16x32_f16 v[190:193], v[186:189], v[214:217], v[190:193]
	v_mfma_f32_16x16x32_f16 v[202:205], v[186:189], v[218:221], v[202:205]
	v_mfma_f32_16x16x32_f16 v[206:209], v[186:189], v[222:225], v[206:209]
	v_mfma_f32_16x16x32_f16 v[186:189], v[186:189], v[226:229], v[210:213]
	s_setprio 0
	s_waitcnt vmcnt(5)
	s_waitcnt lgkmcnt(0)
	s_barrier
	s_nop 0
	ds_read_b128 v[210:213], v131
	ds_read_b128 v[214:217], v131 offset:2048
	ds_read_b128 v[218:221], v131 offset:4096
	ds_read_b128 v[222:225], v131 offset:6144
	ds_read_b128 v[8:11], v129
	ds_read_b128 v[226:229], v129 offset:2048
	s_add_u32 s80, s22, 0x900
	v_lshl_add_u64 v[92:93], s[40:41], 0, v[196:197]
	s_addc_u32 s81, s90, 0
	v_cvt_pk_f16_f32 v7, v6, v7
	s_cmp_lg_u32 s2, 0
	s_cbranch_scc1 .Lres_skip_0
	s_add_u32 m0, s0, 0x18000
	s_nop 0
	global_load_lds_dwordx4 v[92:93], off

.Lres_skip_3:
	v_cvt_pk_f16_f32 v45, v50, v51
	v_cvt_pk_f16_f32 v44, v48, v49
	ds_write_b64 v100, v[44:45] offset:45056
	s_add_u32 s70, s22, 0x60900
	s_addc_u32 s71, s90, 0
	global_load_dwordx4 v[44:47], v201, s[70:71] nt
	s_setprio 1
	s_waitcnt lgkmcnt(1)
	v_mfma_f32_16x16x32_f16 v[16:19], v[238:241], v[210:213], v[16:19]
	v_mfma_f32_16x16x32_f16 v[32:35], v[238:241], v[214:217], v[32:35]
	v_mfma_f32_16x16x32_f16 v[158:161], v[238:241], v[218:221], v[158:161]
	v_mfma_f32_16x16x32_f16 v[166:169], v[238:241], v[222:225], v[166:169]
	v_mfma_f32_16x16x32_f16 v[190:193], v[242:245], v[210:213], v[190:193]
	v_mfma_f32_16x16x32_f16 v[202:205], v[242:245], v[214:217], v[202:205]
	v_mfma_f32_16x16x32_f16 v[206:209], v[242:245], v[218:221], v[206:209]
	v_mfma_f32_16x16x32_f16 v[186:189], v[242:245], v[222:225], v[186:189]
	s_setprio 0
	ds_read_b128 v[210:213], v128
	ds_read_b128 v[214:217], v128 offset:2048
	ds_read_b128 v[218:221], v128 offset:4096
	ds_read_b128 v[222:225], v128 offset:6144
	ds_read_b128 v[238:241], v130
	ds_read_b128 v[242:245], v130 offset:2048
	v_cvt_pk_f16_f32 v49, v54, v55
	v_cvt_pk_f16_f32 v48, v52, v53
	ds_write_b64 v100, v[48:49] offset:49152
	s_add_u32 s70, s22, 0x80900
	s_addc_u32 s71, s90, 0
	global_load_dwordx4 v[48:51], v201, s[70:71] nt
	s_setprio 1
	s_waitcnt lgkmcnt(1)
	v_mfma_f32_16x16x32_f16 v[20:23], v[238:241], v[210:213], v[20:23]
	v_mfma_f32_16x16x32_f16 v[104:107], v[238:241], v[218:221], v[104:107]
	v_mfma_f32_16x16x32_f16 v[108:111], v[242:245], v[210:213], v[108:111]
	v_mfma_f32_16x16x32_f16 v[112:115], v[242:245], v[214:217], v[112:115]
	v_mfma_f32_16x16x32_f16 v[116:119], v[242:245], v[218:221], v[116:119]
	v_mfma_f32_16x16x32_f16 v[230:233], v[238:241], v[214:217], v[230:233]
	v_mfma_f32_16x16x32_f16 v[234:237], v[238:241], v[222:225], v[234:237]
	v_mfma_f32_16x16x32_f16 v[226:229], v[242:245], v[222:225], v[226:229]
	s_setprio 0
	ds_read_b128 v[238:241], v130 offset:4096
	ds_read_b128 v[242:245], v130 offset:6144
	v_cvt_pk_f16_f32 v53, v58, v59
	v_cvt_pk_f16_f32 v52, v56, v57
	ds_write_b64 v100, v[52:53] offset:53248
	s_add_u32 s70, s22, 0xa0900
	s_addc_u32 s71, s90, 0
	global_load_dwordx4 v[52:55], v201, s[70:71] nt
	s_setprio 1
	s_waitcnt lgkmcnt(1)
	v_mfma_f32_16x16x32_f16 v[24:27], v[238:241], v[210:213], v[24:27]
	v_mfma_f32_16x16x32_f16 v[120:123], v[238:241], v[222:225], v[120:123]
	v_mfma_f32_16x16x32_f16 v[124:127], v[242:245], v[210:213], v[124:127]
	v_mfma_f32_16x16x32_f16 v[146:149], v[242:245], v[214:217], v[146:149]
	v_mfma_f32_16x16x32_f16 v[134:137], v[242:245], v[222:225], v[134:137]
	v_mfma_f32_16x16x32_f16 v[138:141], v[238:241], v[214:217], v[138:141]
	v_mfma_f32_16x16x32_f16 v[142:145], v[238:241], v[218:221], v[142:145]
	v_mfma_f32_16x16x32_f16 v[150:153], v[242:245], v[218:221], v[150:153]
	s_setprio 0
	ds_read_b128 v[238:241], v130 offset:8192
	ds_read_b128 v[242:245], v130 offset:10240
	v_cvt_pk_f16_f32 v57, v62, v63
	v_cvt_pk_f16_f32 v56, v60, v61
	ds_write_b64 v100, v[56:57] offset:57344
	s_add_u32 s70, s22, 0xc0900
	s_addc_u32 s71, s90, 0
	global_load_dwordx4 v[56:59], v201, s[70:71] nt
	s_setprio 1
	s_waitcnt lgkmcnt(1)
	v_mfma_f32_16x16x32_f16 v[28:31], v[238:241], v[214:217], v[28:31]
	v_mfma_f32_16x16x32_f16 v[246:249], v[238:241], v[210:213], v[12:15]
	v_mfma_f32_16x16x32_f16 v[170:173], v[238:241], v[218:221], v[170:173]
	v_mfma_f32_16x16x32_f16 v[162:165], v[238:241], v[222:225], v[162:165]
	v_mfma_f32_16x16x32_f16 v[174:177], v[242:245], v[210:213], v[174:177]
	v_mfma_f32_16x16x32_f16 v[178:181], v[242:245], v[214:217], v[178:181]
	v_mfma_f32_16x16x32_f16 v[182:185], v[242:245], v[218:221], v[182:185]
	v_mfma_f32_16x16x32_f16 v[154:157], v[242:245], v[222:225], v[154:157]
	s_setprio 0
	ds_read_b128 v[12:15], v130 offset:12288
	ds_read_b128 v[238:241], v130 offset:14336
	v_cvt_pk_f16_f32 v39, v38, v39
	v_cvt_pk_f16_f32 v38, v36, v37
	ds_write_b64 v100, v[38:39] offset:61440
	s_add_u32 s70, s22, 0xe0900
	s_addc_u32 s71, s90, 0
	global_load_dwordx4 v[60:63], v201, s[70:71] nt
	s_setprio 1
	s_waitcnt lgkmcnt(1)
	v_mfma_f32_16x16x32_f16 v[36:39], v[12:15], v[210:213], v[16:19]
	v_mfma_f32_16x16x32_f16 v[32:35], v[12:15], v[214:217], v[32:35]
	v_mfma_f32_16x16x32_f16 v[158:161], v[12:15], v[218:221], v[158:161]
	v_mfma_f32_16x16x32_f16 v[166:169], v[12:15], v[222:225], v[166:169]
	v_mfma_f32_16x16x32_f16 v[190:193], v[238:241], v[210:213], v[190:193]
	v_mfma_f32_16x16x32_f16 v[202:205], v[238:241], v[214:217], v[202:205]
	v_mfma_f32_16x16x32_f16 v[206:209], v[238:241], v[218:221], v[206:209]
	v_mfma_f32_16x16x32_f16 v[186:189], v[238:241], v[222:225], v[186:189]
	s_setprio 0
	s_waitcnt vmcnt(5)
	s_waitcnt lgkmcnt(0)
	s_barrier
	v_add_u32_e32 v250, 0x20000, v129
	v_add_u32_e32 v251, 0x20000, v130
	ds_read_b128 v[210:213], v131 offset:32768
	ds_read_b128 v[214:217], v131 offset:34816
	ds_read_b128 v[218:221], v131 offset:36864
	ds_read_b128 v[222:225], v131 offset:38912
	ds_read_b128 v[12:15], v250
	ds_read_b128 v[16:19], v250 offset:2048
	s_add_u32 s70, s22, 0xa00
	v_lshl_add_u64 v[92:93], s[42:43], 0, v[196:197]
	s_addc_u32 s71, s90, 0
	s_mov_b32 m0, s1
	v_cvt_pk_f16_f32 v3, v2, v3
	global_load_lds_dwordx4 v[92:93], off
	v_cvt_pk_f16_f32 v2, v0, v1
	ds_write_b64 v100, v[2:3]
	global_load_dwordx4 v[0:3], v201, s[70:71] nt
	s_setprio 1
	s_waitcnt lgkmcnt(1)
	v_mfma_f32_16x16x32_f16 v[104:107], v[12:15], v[218:221], v[104:107]
	v_mfma_f32_16x16x32_f16 v[108:111], v[16:19], v[210:213], v[108:111]
	v_mfma_f32_16x16x32_f16 v[112:115], v[16:19], v[214:217], v[112:115]
	v_mfma_f32_16x16x32_f16 v[116:119], v[16:19], v[218:221], v[116:119]
	v_mfma_f32_16x16x32_f16 v[238:241], v[12:15], v[210:213], v[20:23]
	v_mfma_f32_16x16x32_f16 v[230:233], v[12:15], v[214:217], v[230:233]
	v_mfma_f32_16x16x32_f16 v[234:237], v[12:15], v[222:225], v[234:237]
	v_mfma_f32_16x16x32_f16 v[226:229], v[16:19], v[222:225], v[226:229]
	s_setprio 0
	ds_read_b128 v[16:19], v250 offset:4096
	ds_read_b128 v[20:23], v250 offset:6144
	s_mov_b32 m0, s92
	v_lshl_add_u64 v[12:13], v[92:93], 0, s[58:59]
	global_load_lds_dwordx4 v[12:13], off
	v_cvt_pk_f16_f32 v13, v66, v67
	v_cvt_pk_f16_f32 v12, v64, v65
	ds_write_b64 v100, v[12:13] offset:4096
	s_add_u32 s0, s22, 0x20a00
	s_addc_u32 s1, s90, 0
	global_load_dwordx4 v[12:15], v201, s[0:1] nt
	s_setprio 1
	s_waitcnt lgkmcnt(1)
	v_mfma_f32_16x16x32_f16 v[64:67], v[16:19], v[210:213], v[24:27]
	v_mfma_f32_16x16x32_f16 v[120:123], v[16:19], v[222:225], v[120:123]
	v_mfma_f32_16x16x32_f16 v[124:127], v[20:23], v[210:213], v[124:127]
	v_mfma_f32_16x16x32_f16 v[146:149], v[20:23], v[214:217], v[146:149]
	v_mfma_f32_16x16x32_f16 v[134:137], v[20:23], v[222:225], v[134:137]
	v_mfma_f32_16x16x32_f16 v[138:141], v[16:19], v[214:217], v[138:141]
	v_mfma_f32_16x16x32_f16 v[142:145], v[16:19], v[218:221], v[142:145]
	v_mfma_f32_16x16x32_f16 v[150:153], v[20:23], v[218:221], v[150:153]
	s_setprio 0
	ds_read_b128 v[20:23], v250 offset:8192
	ds_read_b128 v[24:27], v250 offset:10240
	s_mov_b32 m0, s91
	v_lshl_add_u64 v[16:17], v[92:93], 0, s[60:61]
	global_load_lds_dwordx4 v[16:17], off
	v_cvt_pk_f16_f32 v17, v70, v71
	v_cvt_pk_f16_f32 v16, v68, v69
	ds_write_b64 v100, v[16:17] offset:8192
	s_add_u32 s0, s22, 0x40a00
	s_addc_u32 s1, s90, 0
	global_load_dwordx4 v[16:19], v201, s[0:1] nt
	s_setprio 1
	s_waitcnt lgkmcnt(1)
	v_mfma_f32_16x16x32_f16 v[68:71], v[20:23], v[210:213], v[246:249]
	v_mfma_f32_16x16x32_f16 v[242:245], v[20:23], v[214:217], v[28:31]
	v_mfma_f32_16x16x32_f16 v[170:173], v[20:23], v[218:221], v[170:173]
	v_mfma_f32_16x16x32_f16 v[162:165], v[20:23], v[222:225], v[162:165]
	v_mfma_f32_16x16x32_f16 v[174:177], v[24:27], v[210:213], v[174:177]
	v_mfma_f32_16x16x32_f16 v[178:181], v[24:27], v[214:217], v[178:181]
	v_mfma_f32_16x16x32_f16 v[182:185], v[24:27], v[218:221], v[182:185]
	v_mfma_f32_16x16x32_f16 v[154:157], v[24:27], v[222:225], v[154:157]
	s_setprio 0
	ds_read_b128 v[24:27], v250 offset:12288
	ds_read_b128 v[28:31], v250 offset:14336
	s_mov_b32 m0, s73
	v_lshl_add_u64 v[20:21], v[92:93], 0, s[62:63]
	global_load_lds_dwordx4 v[20:21], off
	v_cvt_pk_f16_f32 v21, v74, v75
	v_cvt_pk_f16_f32 v20, v72, v73
	ds_write_b64 v100, v[20:21] offset:12288
	s_add_u32 s0, s22, 0x60a00
	s_addc_u32 s1, s90, 0
	global_load_dwordx4 v[20:23], v201, s[0:1] nt
	s_setprio 1
	s_waitcnt lgkmcnt(1)
	v_mfma_f32_16x16x32_f16 v[72:75], v[24:27], v[210:213], v[36:39]
	v_mfma_f32_16x16x32_f16 v[246:249], v[24:27], v[214:217], v[32:35]
	v_mfma_f32_16x16x32_f16 v[158:161], v[24:27], v[218:221], v[158:161]
	v_mfma_f32_16x16x32_f16 v[166:169], v[24:27], v[222:225], v[166:169]
	v_mfma_f32_16x16x32_f16 v[190:193], v[28:31], v[210:213], v[190:193]
	v_mfma_f32_16x16x32_f16 v[202:205], v[28:31], v[214:217], v[202:205]
	v_mfma_f32_16x16x32_f16 v[206:209], v[28:31], v[218:221], v[206:209]
	v_mfma_f32_16x16x32_f16 v[186:189], v[28:31], v[222:225], v[186:189]
	s_setprio 0
	ds_read_b128 v[210:213], v128 offset:32768
	ds_read_b128 v[214:217], v128 offset:34816
	ds_read_b128 v[218:221], v128 offset:36864
	ds_read_b128 v[222:225], v128 offset:38912
	ds_read_b128 v[28:31], v251
	ds_read_b128 v[32:35], v251 offset:2048
	v_cvt_pk_f16_f32 v25, v78, v79
	v_cvt_pk_f16_f32 v24, v76, v77
	ds_write_b64 v100, v[24:25] offset:16384
	s_add_u32 s0, s22, 0x80a00
	s_addc_u32 s1, s90, 0
	global_load_dwordx4 v[24:27], v201, s[0:1] nt
	s_setprio 1
	s_waitcnt lgkmcnt(1)
	v_mfma_f32_16x16x32_f16 v[76:79], v[28:31], v[210:213], v[238:241]
	v_mfma_f32_16x16x32_f16 v[104:107], v[28:31], v[218:221], v[104:107]
	v_mfma_f32_16x16x32_f16 v[108:111], v[32:35], v[210:213], v[108:111]
	v_mfma_f32_16x16x32_f16 v[112:115], v[32:35], v[214:217], v[112:115]
	v_mfma_f32_16x16x32_f16 v[116:119], v[32:35], v[218:221], v[116:119]
	v_mfma_f32_16x16x32_f16 v[230:233], v[28:31], v[214:217], v[230:233]
	v_mfma_f32_16x16x32_f16 v[234:237], v[28:31], v[222:225], v[234:237]
	v_mfma_f32_16x16x32_f16 v[226:229], v[32:35], v[222:225], v[226:229]
	s_setprio 0
	ds_read_b128 v[32:35], v251 offset:4096
	ds_read_b128 v[36:39], v251 offset:6144
	v_cvt_pk_f16_f32 v29, v82, v83
	v_cvt_pk_f16_f32 v28, v80, v81
	ds_write_b64 v100, v[28:29] offset:20480
	s_add_u32 s0, s22, 0xa0a00
	s_addc_u32 s1, s90, 0
	global_load_dwordx4 v[28:31], v201, s[0:1] nt
	s_setprio 1
	s_waitcnt lgkmcnt(1)
	v_mfma_f32_16x16x32_f16 v[80:83], v[32:35], v[210:213], v[64:67]
	v_mfma_f32_16x16x32_f16 v[120:123], v[32:35], v[222:225], v[120:123]
	v_mfma_f32_16x16x32_f16 v[124:127], v[36:39], v[210:213], v[124:127]
	v_mfma_f32_16x16x32_f16 v[146:149], v[36:39], v[214:217], v[146:149]
	v_mfma_f32_16x16x32_f16 v[134:137], v[36:39], v[222:225], v[134:137]
	v_mfma_f32_16x16x32_f16 v[138:141], v[32:35], v[214:217], v[138:141]
	v_mfma_f32_16x16x32_f16 v[142:145], v[32:35], v[218:221], v[142:145]
	v_mfma_f32_16x16x32_f16 v[150:153], v[36:39], v[218:221], v[150:153]
	s_setprio 0
	ds_read_b128 v[36:39], v251 offset:8192
	ds_read_b128 v[64:67], v251 offset:10240
	v_cvt_pk_f16_f32 v33, v86, v87
	v_cvt_pk_f16_f32 v32, v84, v85
	ds_write_b64 v100, v[32:33] offset:24576
	s_add_u32 s0, s22, 0xc0a00
	s_addc_u32 s1, s90, 0
	global_load_dwordx4 v[32:35], v201, s[0:1] nt
	s_setprio 1
	s_waitcnt lgkmcnt(1)
	v_mfma_f32_16x16x32_f16 v[68:71], v[36:39], v[210:213], v[68:71]
	v_mfma_f32_16x16x32_f16 v[84:87], v[36:39], v[214:217], v[242:245]
	v_mfma_f32_16x16x32_f16 v[170:173], v[36:39], v[218:221], v[170:173]
	v_mfma_f32_16x16x32_f16 v[162:165], v[36:39], v[222:225], v[162:165]
	v_mfma_f32_16x16x32_f16 v[174:177], v[64:67], v[210:213], v[174:177]
	v_mfma_f32_16x16x32_f16 v[178:181], v[64:67], v[214:217], v[178:181]
	v_mfma_f32_16x16x32_f16 v[182:185], v[64:67], v[218:221], v[182:185]
	v_mfma_f32_16x16x32_f16 v[154:157], v[64:67], v[222:225], v[154:157]
	s_setprio 0
	ds_read_b128 v[64:67], v251 offset:12288
	ds_read_b128 v[238:241], v251 offset:14336
	v_cvt_pk_f16_f32 v37, v90, v91
	v_cvt_pk_f16_f32 v36, v88, v89
	ds_write_b64 v100, v[36:37] offset:28672
	s_add_u32 s0, s22, 0xe0a00
	s_addc_u32 s1, s90, 0
	global_load_dwordx4 v[36:39], v201, s[0:1] nt
	s_setprio 1
	s_waitcnt lgkmcnt(1)
	v_mfma_f32_16x16x32_f16 v[72:75], v[64:67], v[210:213], v[72:75]
	v_mfma_f32_16x16x32_f16 v[88:91], v[64:67], v[214:217], v[246:249]
	v_mfma_f32_16x16x32_f16 v[158:161], v[64:67], v[218:221], v[158:161]
	v_mfma_f32_16x16x32_f16 v[166:169], v[64:67], v[222:225], v[166:169]
	v_mfma_f32_16x16x32_f16 v[190:193], v[238:241], v[210:213], v[190:193]
	v_mfma_f32_16x16x32_f16 v[202:205], v[238:241], v[214:217], v[202:205]
	v_mfma_f32_16x16x32_f16 v[206:209], v[238:241], v[218:221], v[206:209]
	v_mfma_f32_16x16x32_f16 v[186:189], v[238:241], v[222:225], v[186:189]
	s_setprio 0
	s_waitcnt vmcnt(5)
	s_waitcnt lgkmcnt(0)
	s_barrier
	ds_read_b128 v[210:213], v131
	ds_read_b128 v[214:217], v131 offset:2048
	ds_read_b128 v[218:221], v131 offset:4096
	ds_read_b128 v[222:225], v131 offset:6144
	ds_read_b128 v[64:67], v129
	ds_read_b128 v[238:241], v129 offset:2048
	s_add_u32 s70, s22, 0xb00
	v_lshl_add_u64 v[92:93], s[44:45], 0, v[196:197]
	s_addc_u32 s71, s90, 0
	v_readfirstlane_b32 s0, v95
	s_mov_b32 m0, s0
	v_cvt_pk_f16_f32 v7, v6, v7
	global_load_lds_dwordx4 v[92:93], off
	v_cvt_pk_f16_f32 v6, v4, v5
	ds_write_b64 v100, v[6:7] offset:32768
	global_load_dwordx4 v[4:7], v201, s[70:71] nt
	s_setprio 1
	s_waitcnt lgkmcnt(1)
	v_mfma_f32_16x16x32_f16 v[76:79], v[64:67], v[210:213], v[76:79]
	v_mfma_f32_16x16x32_f16 v[104:107], v[64:67], v[218:221], v[104:107]
	v_mfma_f32_16x16x32_f16 v[108:111], v[238:241], v[210:213], v[108:111]
	v_mfma_f32_16x16x32_f16 v[112:115], v[238:241], v[214:217], v[112:115]
	v_mfma_f32_16x16x32_f16 v[116:119], v[238:241], v[218:221], v[116:119]
	v_mfma_f32_16x16x32_f16 v[230:233], v[64:67], v[214:217], v[230:233]
	v_mfma_f32_16x16x32_f16 v[234:237], v[64:67], v[222:225], v[234:237]
	v_mfma_f32_16x16x32_f16 v[226:229], v[238:241], v[222:225], v[226:229]
	s_setprio 0
	ds_read_b128 v[238:241], v129 offset:4096
	ds_read_b128 v[242:245], v129 offset:6144
	v_readfirstlane_b32 s72, v96
	v_lshl_add_u64 v[64:65], v[92:93], 0, s[58:59]
	s_mov_b32 m0, s72
	v_cvt_pk_f16_f32 v11, v10, v11
	global_load_lds_dwordx4 v[64:65], off
	v_cvt_pk_f16_f32 v10, v8, v9
	ds_write_b64 v100, v[10:11] offset:36864
	s_add_u32 s70, s22, 0x20b00
	s_addc_u32 s71, s90, 0
	global_load_dwordx4 v[64:67], v201, s[70:71] nt
	s_setprio 1
	s_waitcnt lgkmcnt(1)
	v_mfma_f32_16x16x32_f16 v[8:11], v[238:241], v[210:213], v[80:83]
	v_mfma_f32_16x16x32_f16 v[80:83], v[238:241], v[214:217], v[138:141]
	v_mfma_f32_16x16x32_f16 v[138:141], v[238:241], v[218:221], v[142:145]
	v_mfma_f32_16x16x32_f16 v[120:123], v[238:241], v[222:225], v[120:123]
	v_mfma_f32_16x16x32_f16 v[124:127], v[242:245], v[210:213], v[124:127]
	v_mfma_f32_16x16x32_f16 v[142:145], v[242:245], v[214:217], v[146:149]
	v_mfma_f32_16x16x32_f16 v[146:149], v[242:245], v[218:221], v[150:153]
	v_mfma_f32_16x16x32_f16 v[134:137], v[242:245], v[222:225], v[134:137]
	s_setprio 0
	s_nop 0
	ds_read_b128 v[150:153], v129 offset:8192
	ds_read_b128 v[238:241], v129 offset:10240
	v_readfirstlane_b32 s71, v97
	v_lshl_add_u64 v[198:199], v[92:93], 0, s[60:61]
	s_mov_b32 m0, s71
	v_cvt_pk_f16_f32 v43, v42, v43
	global_load_lds_dwordx4 v[198:199], off
	v_cvt_pk_f16_f32 v42, v40, v41
	ds_write_b64 v100, v[42:43] offset:40960
	s_add_u32 s80, s22, 0x40b00
	s_addc_u32 s81, s90, 0
	global_load_dwordx4 v[40:43], v201, s[80:81] nt
	s_setprio 1
	s_waitcnt lgkmcnt(1)
	v_mfma_f32_16x16x32_f16 v[68:71], v[150:153], v[210:213], v[68:71]
	v_mfma_f32_16x16x32_f16 v[84:87], v[150:153], v[214:217], v[84:87]
	v_mfma_f32_16x16x32_f16 v[170:173], v[150:153], v[218:221], v[170:173]
	v_mfma_f32_16x16x32_f16 v[150:153], v[150:153], v[222:225], v[162:165]
	v_mfma_f32_16x16x32_f16 v[162:165], v[238:241], v[210:213], v[174:177]
	v_mfma_f32_16x16x32_f16 v[174:177], v[238:241], v[214:217], v[178:181]
	v_mfma_f32_16x16x32_f16 v[178:181], v[238:241], v[218:221], v[182:185]
	v_mfma_f32_16x16x32_f16 v[154:157], v[238:241], v[222:225], v[154:157]
	s_setprio 0
	s_nop 0
	ds_read_b128 v[182:185], v129 offset:12288
	ds_read_b128 v[238:241], v129 offset:14336
	v_readfirstlane_b32 s70, v98
	v_lshl_add_u64 v[92:93], v[92:93], 0, s[62:63]
	s_mov_b32 m0, s70
	v_cvt_pk_f16_f32 v47, v46, v47
	global_load_lds_dwordx4 v[92:93], off
	v_cvt_pk_f16_f32 v46, v44, v45
	ds_write_b64 v100, v[46:47] offset:45056
	s_add_u32 s80, s22, 0x60b00
	s_addc_u32 s81, s90, 0
	global_load_dwordx4 v[44:47], v201, s[80:81] nt
	s_setprio 1
	s_waitcnt lgkmcnt(1)
	v_mfma_f32_16x16x32_f16 v[72:75], v[182:185], v[210:213], v[72:75]
	v_mfma_f32_16x16x32_f16 v[88:91], v[182:185], v[214:217], v[88:91]
	v_mfma_f32_16x16x32_f16 v[158:161], v[182:185], v[218:221], v[158:161]
	v_mfma_f32_16x16x32_f16 v[166:169], v[182:185], v[222:225], v[166:169]
	v_mfma_f32_16x16x32_f16 v[182:185], v[238:241], v[210:213], v[190:193]
	v_mfma_f32_16x16x32_f16 v[190:193], v[238:241], v[214:217], v[202:205]
	v_mfma_f32_16x16x32_f16 v[202:205], v[238:241], v[218:221], v[206:209]
	v_mfma_f32_16x16x32_f16 v[186:189], v[238:241], v[222:225], v[186:189]
	s_setprio 0
	s_nop 0
	ds_read_b128 v[206:209], v128
	ds_read_b128 v[210:213], v128 offset:2048
	ds_read_b128 v[214:217], v128 offset:4096
	ds_read_b128 v[218:221], v128 offset:6144
	ds_read_b128 v[222:225], v130
	ds_read_b128 v[238:241], v130 offset:2048
	v_cvt_pk_f16_f32 v51, v50, v51
	v_cvt_pk_f16_f32 v50, v48, v49
	ds_write_b64 v100, v[50:51] offset:49152
	s_add_u32 s80, s22, 0x80b00
	s_addc_u32 s81, s90, 0
	global_load_dwordx4 v[48:51], v201, s[80:81] nt
	s_setprio 1
	s_waitcnt lgkmcnt(1)
	v_mfma_f32_16x16x32_f16 v[76:79], v[222:225], v[206:209], v[76:79]
	v_mfma_f32_16x16x32_f16 v[104:107], v[222:225], v[214:217], v[104:107]
	v_mfma_f32_16x16x32_f16 v[108:111], v[238:241], v[206:209], v[108:111]
	v_mfma_f32_16x16x32_f16 v[112:115], v[238:241], v[210:213], v[112:115]
	v_mfma_f32_16x16x32_f16 v[116:119], v[238:241], v[214:217], v[116:119]
	v_mfma_f32_16x16x32_f16 v[230:233], v[222:225], v[210:213], v[230:233]
	v_mfma_f32_16x16x32_f16 v[222:225], v[222:225], v[218:221], v[234:237]
	v_mfma_f32_16x16x32_f16 v[226:229], v[238:241], v[218:221], v[226:229]
	s_setprio 0
	s_nop 0
	ds_read_b128 v[234:237], v130 offset:4096
	ds_read_b128 v[238:241], v130 offset:6144
	v_cvt_pk_f16_f32 v55, v54, v55
	v_cvt_pk_f16_f32 v54, v52, v53
	ds_write_b64 v100, v[54:55] offset:53248
	s_add_u32 s80, s22, 0xa0b00
	s_addc_u32 s81, s90, 0
	global_load_dwordx4 v[52:55], v201, s[80:81] nt
	s_setprio 1
	s_waitcnt lgkmcnt(1)
	v_mfma_f32_16x16x32_f16 v[80:83], v[234:237], v[210:213], v[80:83]
	v_mfma_f32_16x16x32_f16 v[120:123], v[234:237], v[218:221], v[120:123]
	v_mfma_f32_16x16x32_f16 v[124:127], v[238:241], v[206:209], v[124:127]
	v_mfma_f32_16x16x32_f16 v[146:149], v[238:241], v[214:217], v[146:149]
	v_mfma_f32_16x16x32_f16 v[134:137], v[238:241], v[218:221], v[134:137]
	v_mfma_f32_16x16x32_f16 v[242:245], v[234:237], v[206:209], v[8:11]
	v_mfma_f32_16x16x32_f16 v[138:141], v[234:237], v[214:217], v[138:141]
	v_mfma_f32_16x16x32_f16 v[142:145], v[238:241], v[210:213], v[142:145]
	s_setprio 0
	ds_read_b128 v[8:11], v130 offset:8192
	ds_read_b128 v[234:237], v130 offset:10240
	v_cvt_pk_f16_f32 v59, v58, v59
	v_cvt_pk_f16_f32 v58, v56, v57
	ds_write_b64 v100, v[58:59] offset:57344
	s_add_u32 s80, s22, 0xc0b00
	s_addc_u32 s81, s90, 0
	global_load_dwordx4 v[56:59], v201, s[80:81] nt
	s_setprio 1
	s_waitcnt lgkmcnt(1)
	v_mfma_f32_16x16x32_f16 v[84:87], v[8:11], v[210:213], v[84:87]
	v_mfma_f32_16x16x32_f16 v[238:241], v[8:11], v[206:209], v[68:71]
	v_mfma_f32_16x16x32_f16 v[170:173], v[8:11], v[214:217], v[170:173]
	v_mfma_f32_16x16x32_f16 v[150:153], v[8:11], v[218:221], v[150:153]
	v_mfma_f32_16x16x32_f16 v[162:165], v[234:237], v[206:209], v[162:165]
	v_mfma_f32_16x16x32_f16 v[174:177], v[234:237], v[210:213], v[174:177]
	v_mfma_f32_16x16x32_f16 v[178:181], v[234:237], v[214:217], v[178:181]
	v_mfma_f32_16x16x32_f16 v[154:157], v[234:237], v[218:221], v[154:157]
	s_setprio 0
	ds_read_b128 v[8:11], v130 offset:12288
	ds_read_b128 v[68:71], v130 offset:14336
	v_cvt_pk_f16_f32 v63, v62, v63
	v_cvt_pk_f16_f32 v62, v60, v61
	ds_write_b64 v100, v[62:63] offset:61440
	s_add_u32 s80, s22, 0xe0b00
	s_addc_u32 s81, s90, 0
	global_load_dwordx4 v[60:63], v201, s[80:81] nt
	s_setprio 1
	s_waitcnt lgkmcnt(1)
	v_mfma_f32_16x16x32_f16 v[88:91], v[8:11], v[210:213], v[88:91]
	v_mfma_f32_16x16x32_f16 v[234:237], v[8:11], v[206:209], v[72:75]
	v_mfma_f32_16x16x32_f16 v[158:161], v[8:11], v[214:217], v[158:161]
	v_mfma_f32_16x16x32_f16 v[166:169], v[8:11], v[218:221], v[166:169]
	v_mfma_f32_16x16x32_f16 v[182:185], v[68:71], v[206:209], v[182:185]
	v_mfma_f32_16x16x32_f16 v[190:193], v[68:71], v[210:213], v[190:193]
	v_mfma_f32_16x16x32_f16 v[202:205], v[68:71], v[214:217], v[202:205]
	v_mfma_f32_16x16x32_f16 v[186:189], v[68:71], v[218:221], v[186:189]
	s_setprio 0
	s_waitcnt vmcnt(5)
	s_waitcnt lgkmcnt(0)
	s_barrier
	ds_read_b128 v[206:209], v131 offset:32768
	ds_read_b128 v[210:213], v131 offset:34816
	ds_read_b128 v[214:217], v131 offset:36864
	ds_read_b128 v[218:221], v131 offset:38912
	ds_read_b128 v[68:71], v129 offset:32768
	ds_read_b128 v[72:75], v129 offset:34816
	s_add_u32 s80, s22, 0xc00
	v_lshl_add_u64 v[92:93], s[46:47], 0, v[196:197]
	s_addc_u32 s81, s90, 0
	v_readfirstlane_b32 s1, v94
	s_mov_b32 m0, s1
	v_cvt_pk_f16_f32 v3, v2, v3
	global_load_lds_dwordx4 v[92:93], off
	v_cvt_pk_f16_f32 v2, v0, v1
	ds_write_b64 v100, v[2:3]
	global_load_dwordx4 v[8:11], v201, s[80:81] nt
	s_setprio 1
	s_waitcnt lgkmcnt(1)
	v_mfma_f32_16x16x32_f16 v[0:3], v[68:71], v[206:209], v[76:79]
	v_mfma_f32_16x16x32_f16 v[104:107], v[68:71], v[214:217], v[104:107]
	v_mfma_f32_16x16x32_f16 v[108:111], v[72:75], v[206:209], v[108:111]
	v_mfma_f32_16x16x32_f16 v[112:115], v[72:75], v[210:213], v[112:115]
	v_mfma_f32_16x16x32_f16 v[116:119], v[72:75], v[214:217], v[116:119]
	v_mfma_f32_16x16x32_f16 v[230:233], v[68:71], v[210:213], v[230:233]
	v_mfma_f32_16x16x32_f16 v[222:225], v[68:71], v[218:221], v[222:225]
	v_mfma_f32_16x16x32_f16 v[226:229], v[72:75], v[218:221], v[226:229]
	s_setprio 0
	ds_read_b128 v[72:75], v129 offset:36864
	ds_read_b128 v[76:79], v129 offset:38912
	v_readfirstlane_b32 s92, v99
	v_lshl_add_u64 v[68:69], v[92:93], 0, s[58:59]
	s_mov_b32 m0, s92
	v_cvt_pk_f16_f32 v15, v14, v15
	global_load_lds_dwordx4 v[68:69], off
	v_cvt_pk_f16_f32 v14, v12, v13
	ds_write_b64 v100, v[14:15] offset:4096
	s_add_u32 s80, s22, 0x20c00
	s_addc_u32 s81, s90, 0
	global_load_dwordx4 v[68:71], v201, s[80:81] nt
	s_setprio 1
	s_waitcnt lgkmcnt(1)
	v_mfma_f32_16x16x32_f16 v[12:15], v[72:75], v[206:209], v[242:245]
	v_mfma_f32_16x16x32_f16 v[120:123], v[72:75], v[218:221], v[120:123]
	v_mfma_f32_16x16x32_f16 v[124:127], v[76:79], v[206:209], v[124:127]
	v_mfma_f32_16x16x32_f16 v[146:149], v[76:79], v[214:217], v[146:149]
	v_mfma_f32_16x16x32_f16 v[134:137], v[76:79], v[218:221], v[134:137]
	v_mfma_f32_16x16x32_f16 v[242:245], v[72:75], v[210:213], v[80:83]
	v_mfma_f32_16x16x32_f16 v[138:141], v[72:75], v[214:217], v[138:141]
	v_mfma_f32_16x16x32_f16 v[142:145], v[76:79], v[210:213], v[142:145]
	s_setprio 0
	ds_read_b128 v[76:79], v129 offset:40960
	ds_read_b128 v[80:83], v129 offset:43008
	v_readfirstlane_b32 s91, v101
	v_lshl_add_u64 v[72:73], v[92:93], 0, s[60:61]
	s_mov_b32 m0, s91
	v_cvt_pk_f16_f32 v19, v18, v19
	global_load_lds_dwordx4 v[72:73], off
	v_cvt_pk_f16_f32 v18, v16, v17
	ds_write_b64 v100, v[18:19] offset:8192
	s_add_u32 s80, s22, 0x40c00
	s_addc_u32 s81, s90, 0
	global_load_dwordx4 v[72:75], v201, s[80:81] nt
	s_setprio 1
	s_waitcnt lgkmcnt(1)
	v_mfma_f32_16x16x32_f16 v[16:19], v[76:79], v[206:209], v[238:241]
	v_mfma_f32_16x16x32_f16 v[238:241], v[76:79], v[210:213], v[84:87]
	v_mfma_f32_16x16x32_f16 v[170:173], v[76:79], v[214:217], v[170:173]
	v_mfma_f32_16x16x32_f16 v[150:153], v[76:79], v[218:221], v[150:153]
	v_mfma_f32_16x16x32_f16 v[162:165], v[80:83], v[206:209], v[162:165]
	v_mfma_f32_16x16x32_f16 v[174:177], v[80:83], v[210:213], v[174:177]
	v_mfma_f32_16x16x32_f16 v[178:181], v[80:83], v[214:217], v[178:181]
	v_mfma_f32_16x16x32_f16 v[154:157], v[80:83], v[218:221], v[154:157]
	s_setprio 0
	ds_read_b128 v[80:83], v129 offset:45056
	ds_read_b128 v[84:87], v129 offset:47104
	v_readfirstlane_b32 s73, v102
	v_lshl_add_u64 v[76:77], v[92:93], 0, s[62:63]
	s_mov_b32 m0, s73
	v_cvt_pk_f16_f32 v23, v22, v23
	global_load_lds_dwordx4 v[76:77], off
	v_cvt_pk_f16_f32 v22, v20, v21
	ds_write_b64 v100, v[22:23] offset:12288
	s_add_u32 s80, s22, 0x60c00
	s_addc_u32 s81, s90, 0
	global_load_dwordx4 v[76:79], v201, s[80:81] nt
	s_setprio 1
	s_waitcnt lgkmcnt(1)
	v_mfma_f32_16x16x32_f16 v[20:23], v[80:83], v[206:209], v[234:237]
	v_mfma_f32_16x16x32_f16 v[234:237], v[80:83], v[210:213], v[88:91]
	v_mfma_f32_16x16x32_f16 v[158:161], v[80:83], v[214:217], v[158:161]
	v_mfma_f32_16x16x32_f16 v[166:169], v[80:83], v[218:221], v[166:169]
	v_mfma_f32_16x16x32_f16 v[182:185], v[84:87], v[206:209], v[182:185]
	v_mfma_f32_16x16x32_f16 v[190:193], v[84:87], v[210:213], v[190:193]
	v_mfma_f32_16x16x32_f16 v[202:205], v[84:87], v[214:217], v[202:205]
	v_mfma_f32_16x16x32_f16 v[186:189], v[84:87], v[218:221], v[186:189]
	s_setprio 0
	ds_read_b128 v[206:209], v128 offset:32768
	ds_read_b128 v[210:213], v128 offset:34816
	ds_read_b128 v[214:217], v128 offset:36864
	ds_read_b128 v[218:221], v128 offset:38912
	ds_read_b128 v[84:87], v130 offset:32768
	ds_read_b128 v[88:91], v130 offset:34816
	v_cvt_pk_f16_f32 v27, v26, v27
	v_cvt_pk_f16_f32 v26, v24, v25
	ds_write_b64 v100, v[26:27] offset:16384
	s_add_u32 s80, s22, 0x80c00
	s_addc_u32 s81, s90, 0
	global_load_dwordx4 v[80:83], v201, s[80:81] nt
	s_setprio 1
	s_waitcnt lgkmcnt(1)
	v_mfma_f32_16x16x32_f16 v[24:27], v[84:87], v[206:209], v[0:3]
	v_mfma_f32_16x16x32_f16 v[104:107], v[84:87], v[214:217], v[104:107]
	v_mfma_f32_16x16x32_f16 v[108:111], v[88:91], v[206:209], v[108:111]
	v_mfma_f32_16x16x32_f16 v[112:115], v[88:91], v[210:213], v[112:115]
	v_mfma_f32_16x16x32_f16 v[116:119], v[88:91], v[214:217], v[116:119]
	v_mfma_f32_16x16x32_f16 v[230:233], v[84:87], v[210:213], v[230:233]
	v_mfma_f32_16x16x32_f16 v[222:225], v[84:87], v[218:221], v[222:225]
	v_mfma_f32_16x16x32_f16 v[226:229], v[88:91], v[218:221], v[226:229]
	s_setprio 0
	ds_read_b128 v[0:3], v130 offset:36864
	ds_read_b128 v[88:91], v130 offset:38912
	v_cvt_pk_f16_f32 v31, v30, v31
	v_cvt_pk_f16_f32 v30, v28, v29
	ds_write_b64 v100, v[30:31] offset:20480
	s_add_u32 s80, s22, 0xa0c00
	s_addc_u32 s81, s90, 0
	global_load_dwordx4 v[84:87], v201, s[80:81] nt
	s_setprio 1
	s_waitcnt lgkmcnt(1)
	v_mfma_f32_16x16x32_f16 v[12:15], v[0:3], v[206:209], v[12:15]
	v_mfma_f32_16x16x32_f16 v[28:31], v[0:3], v[210:213], v[242:245]
	v_mfma_f32_16x16x32_f16 v[120:123], v[0:3], v[218:221], v[120:123]
	v_mfma_f32_16x16x32_f16 v[124:127], v[88:91], v[206:209], v[124:127]
	v_mfma_f32_16x16x32_f16 v[146:149], v[88:91], v[214:217], v[146:149]
	v_mfma_f32_16x16x32_f16 v[134:137], v[88:91], v[218:221], v[134:137]
	v_mfma_f32_16x16x32_f16 v[138:141], v[0:3], v[214:217], v[138:141]
	v_mfma_f32_16x16x32_f16 v[142:145], v[88:91], v[210:213], v[142:145]
	s_setprio 0
	ds_read_b128 v[0:3], v130 offset:40960
	ds_read_b128 v[242:245], v130 offset:43008
	v_cvt_pk_f16_f32 v35, v34, v35
	v_cvt_pk_f16_f32 v34, v32, v33
	ds_write_b64 v100, v[34:35] offset:24576
	s_add_u32 s80, s22, 0xc0c00
	s_addc_u32 s81, s90, 0
	global_load_dwordx4 v[88:91], v201, s[80:81] nt
	s_setprio 1
	s_waitcnt lgkmcnt(1)
	v_mfma_f32_16x16x32_f16 v[16:19], v[0:3], v[206:209], v[16:19]
	v_mfma_f32_16x16x32_f16 v[32:35], v[0:3], v[210:213], v[238:241]
	v_mfma_f32_16x16x32_f16 v[170:173], v[0:3], v[214:217], v[170:173]
	v_mfma_f32_16x16x32_f16 v[150:153], v[0:3], v[218:221], v[150:153]
	v_mfma_f32_16x16x32_f16 v[162:165], v[242:245], v[206:209], v[162:165]
	v_mfma_f32_16x16x32_f16 v[174:177], v[242:245], v[210:213], v[174:177]
	v_mfma_f32_16x16x32_f16 v[178:181], v[242:245], v[214:217], v[178:181]
	v_mfma_f32_16x16x32_f16 v[154:157], v[242:245], v[218:221], v[154:157]
	s_setprio 0
	ds_read_b128 v[0:3], v130 offset:45056
	ds_read_b128 v[238:241], v130 offset:47104
	v_cvt_pk_f16_f32 v39, v38, v39
	v_cvt_pk_f16_f32 v38, v36, v37
	ds_write_b64 v100, v[38:39] offset:28672
	s_add_u32 s80, s22, 0xe0c00
	s_addc_u32 s81, s90, 0
	global_load_dwordx4 v[36:39], v201, s[80:81] nt
	s_setprio 1
	s_waitcnt lgkmcnt(1)
	v_mfma_f32_16x16x32_f16 v[20:23], v[0:3], v[206:209], v[20:23]
	v_mfma_f32_16x16x32_f16 v[234:237], v[0:3], v[210:213], v[234:237]
	v_mfma_f32_16x16x32_f16 v[158:161], v[0:3], v[214:217], v[158:161]
	v_mfma_f32_16x16x32_f16 v[166:169], v[0:3], v[218:221], v[166:169]
	v_mfma_f32_16x16x32_f16 v[182:185], v[238:241], v[206:209], v[182:185]
	v_mfma_f32_16x16x32_f16 v[190:193], v[238:241], v[210:213], v[190:193]
	v_mfma_f32_16x16x32_f16 v[202:205], v[238:241], v[214:217], v[202:205]
	v_mfma_f32_16x16x32_f16 v[186:189], v[238:241], v[218:221], v[186:189]
	s_setprio 0
	s_waitcnt vmcnt(5)
	s_waitcnt lgkmcnt(0)
	s_barrier
	ds_read_b128 v[206:209], v131
	ds_read_b128 v[210:213], v131 offset:2048
	ds_read_b128 v[214:217], v131 offset:4096
	ds_read_b128 v[218:221], v131 offset:6144
	ds_read_b128 v[238:241], v129
	ds_read_b128 v[242:245], v129 offset:2048
	s_add_u32 s80, s22, 0xd00
	v_lshl_add_u64 v[92:93], s[48:49], 0, v[196:197]
	s_addc_u32 s81, s90, 0
	s_mov_b32 m0, s0
	v_cvt_pk_f16_f32 v1, v6, v7
	global_load_lds_dwordx4 v[92:93], off
	v_cvt_pk_f16_f32 v0, v4, v5
	ds_write_b64 v100, v[0:1] offset:32768
	global_load_dwordx4 v[0:3], v201, s[80:81] nt
	s_setprio 1
	s_waitcnt lgkmcnt(1)
	v_mfma_f32_16x16x32_f16 v[24:27], v[238:241], v[206:209], v[24:27]
	v_mfma_f32_16x16x32_f16 v[104:107], v[238:241], v[214:217], v[104:107]
	v_mfma_f32_16x16x32_f16 v[108:111], v[242:245], v[206:209], v[108:111]
	v_mfma_f32_16x16x32_f16 v[112:115], v[242:245], v[210:213], v[112:115]
	v_mfma_f32_16x16x32_f16 v[116:119], v[242:245], v[214:217], v[116:119]
	v_mfma_f32_16x16x32_f16 v[230:233], v[238:241], v[210:213], v[230:233]
	v_mfma_f32_16x16x32_f16 v[222:225], v[238:241], v[218:221], v[222:225]
	v_mfma_f32_16x16x32_f16 v[226:229], v[242:245], v[218:221], v[226:229]
	s_setprio 0
	ds_read_b128 v[238:241], v129 offset:4096
	ds_read_b128 v[242:245], v129 offset:6144
	s_mov_b32 m0, s72
	v_lshl_add_u64 v[4:5], v[92:93], 0, s[58:59]
	global_load_lds_dwordx4 v[4:5], off
	v_cvt_pk_f16_f32 v5, v66, v67
	v_cvt_pk_f16_f32 v4, v64, v65
	ds_write_b64 v100, v[4:5] offset:36864
	s_add_u32 s80, s22, 0x20d00
	s_addc_u32 s81, s90, 0
	global_load_dwordx4 v[4:7], v201, s[80:81] nt
	s_setprio 1
	s_waitcnt lgkmcnt(1)
	v_mfma_f32_16x16x32_f16 v[64:67], v[238:241], v[206:209], v[12:15]
	v_mfma_f32_16x16x32_f16 v[28:31], v[238:241], v[210:213], v[28:31]
	v_mfma_f32_16x16x32_f16 v[120:123], v[238:241], v[218:221], v[120:123]
	v_mfma_f32_16x16x32_f16 v[124:127], v[242:245], v[206:209], v[124:127]
	v_mfma_f32_16x16x32_f16 v[146:149], v[242:245], v[214:217], v[146:149]
	v_mfma_f32_16x16x32_f16 v[134:137], v[242:245], v[218:221], v[134:137]
	v_mfma_f32_16x16x32_f16 v[138:141], v[238:241], v[214:217], v[138:141]
	v_mfma_f32_16x16x32_f16 v[142:145], v[242:245], v[210:213], v[142:145]
	s_setprio 0
	ds_read_b128 v[238:241], v129 offset:8192
	ds_read_b128 v[242:245], v129 offset:10240
	s_mov_b32 m0, s71
	v_lshl_add_u64 v[12:13], v[92:93], 0, s[60:61]
	global_load_lds_dwordx4 v[12:13], off
	v_cvt_pk_f16_f32 v13, v42, v43
	v_cvt_pk_f16_f32 v12, v40, v41
	ds_write_b64 v100, v[12:13] offset:40960
	s_add_u32 s80, s22, 0x40d00
	s_addc_u32 s81, s90, 0
	global_load_dwordx4 v[12:15], v201, s[80:81] nt
	s_setprio 1
	s_waitcnt lgkmcnt(1)
	v_mfma_f32_16x16x32_f16 v[40:43], v[238:241], v[206:209], v[16:19]
	v_mfma_f32_16x16x32_f16 v[32:35], v[238:241], v[210:213], v[32:35]
	v_mfma_f32_16x16x32_f16 v[170:173], v[238:241], v[214:217], v[170:173]
	v_mfma_f32_16x16x32_f16 v[150:153], v[238:241], v[218:221], v[150:153]
	v_mfma_f32_16x16x32_f16 v[162:165], v[242:245], v[206:209], v[162:165]
	v_mfma_f32_16x16x32_f16 v[174:177], v[242:245], v[210:213], v[174:177]
	v_mfma_f32_16x16x32_f16 v[178:181], v[242:245], v[214:217], v[178:181]
	v_mfma_f32_16x16x32_f16 v[154:157], v[242:245], v[218:221], v[154:157]
	s_setprio 0
	ds_read_b128 v[238:241], v129 offset:12288
	ds_read_b128 v[242:245], v129 offset:14336
	s_mov_b32 m0, s70
	v_lshl_add_u64 v[16:17], v[92:93], 0, s[62:63]
	global_load_lds_dwordx4 v[16:17], off
	v_cvt_pk_f16_f32 v17, v46, v47
	v_cvt_pk_f16_f32 v16, v44, v45
	ds_write_b64 v100, v[16:17] offset:45056
	s_add_u32 s70, s22, 0x60d00
	s_addc_u32 s71, s90, 0
	global_load_dwordx4 v[16:19], v201, s[70:71] nt
	s_setprio 1
	s_waitcnt lgkmcnt(1)
	v_mfma_f32_16x16x32_f16 v[44:47], v[238:241], v[206:209], v[20:23]
	v_mfma_f32_16x16x32_f16 v[234:237], v[238:241], v[210:213], v[234:237]
	v_mfma_f32_16x16x32_f16 v[158:161], v[238:241], v[214:217], v[158:161]
	v_mfma_f32_16x16x32_f16 v[166:169], v[238:241], v[218:221], v[166:169]
	v_mfma_f32_16x16x32_f16 v[182:185], v[242:245], v[206:209], v[182:185]
	v_mfma_f32_16x16x32_f16 v[190:193], v[242:245], v[210:213], v[190:193]
	v_mfma_f32_16x16x32_f16 v[202:205], v[242:245], v[214:217], v[202:205]
	v_mfma_f32_16x16x32_f16 v[186:189], v[242:245], v[218:221], v[186:189]
	s_setprio 0
	ds_read_b128 v[206:209], v128
	ds_read_b128 v[210:213], v128 offset:2048
	ds_read_b128 v[214:217], v128 offset:4096
	ds_read_b128 v[218:221], v128 offset:6144
	ds_read_b128 v[238:241], v130
	ds_read_b128 v[242:245], v130 offset:2048
	v_cvt_pk_f16_f32 v21, v50, v51
	v_cvt_pk_f16_f32 v20, v48, v49
	ds_write_b64 v100, v[20:21] offset:49152
	s_add_u32 s70, s22, 0x80d00
	s_addc_u32 s71, s90, 0
	global_load_dwordx4 v[20:23], v201, s[70:71] nt
	s_setprio 1
	s_waitcnt lgkmcnt(1)
	v_mfma_f32_16x16x32_f16 v[48:51], v[238:241], v[206:209], v[24:27]
	v_mfma_f32_16x16x32_f16 v[104:107], v[238:241], v[214:217], v[104:107]
	v_mfma_f32_16x16x32_f16 v[108:111], v[242:245], v[206:209], v[108:111]
	v_mfma_f32_16x16x32_f16 v[112:115], v[242:245], v[210:213], v[112:115]
	v_mfma_f32_16x16x32_f16 v[116:119], v[242:245], v[214:217], v[116:119]
	v_mfma_f32_16x16x32_f16 v[230:233], v[238:241], v[210:213], v[230:233]
	v_mfma_f32_16x16x32_f16 v[222:225], v[238:241], v[218:221], v[222:225]
	v_mfma_f32_16x16x32_f16 v[226:229], v[242:245], v[218:221], v[226:229]
	s_setprio 0
	ds_read_b128 v[238:241], v130 offset:4096
	ds_read_b128 v[242:245], v130 offset:6144
	v_cvt_pk_f16_f32 v25, v54, v55
	v_cvt_pk_f16_f32 v24, v52, v53
	ds_write_b64 v100, v[24:25] offset:53248
	s_add_u32 s70, s22, 0xa0d00
	s_addc_u32 s71, s90, 0
	global_load_dwordx4 v[24:27], v201, s[70:71] nt
	s_setprio 1
	s_waitcnt lgkmcnt(1)
	v_mfma_f32_16x16x32_f16 v[52:55], v[238:241], v[206:209], v[64:67]
	v_mfma_f32_16x16x32_f16 v[64:67], v[238:241], v[210:213], v[28:31]
	v_mfma_f32_16x16x32_f16 v[120:123], v[238:241], v[218:221], v[120:123]
	v_mfma_f32_16x16x32_f16 v[124:127], v[242:245], v[206:209], v[124:127]
	v_mfma_f32_16x16x32_f16 v[146:149], v[242:245], v[214:217], v[146:149]
	v_mfma_f32_16x16x32_f16 v[134:137], v[242:245], v[218:221], v[134:137]
	v_mfma_f32_16x16x32_f16 v[138:141], v[238:241], v[214:217], v[138:141]
	v_mfma_f32_16x16x32_f16 v[142:145], v[242:245], v[210:213], v[142:145]
	s_setprio 0
	ds_read_b128 v[238:241], v130 offset:8192
	ds_read_b128 v[242:245], v130 offset:10240
	v_cvt_pk_f16_f32 v29, v58, v59
	v_cvt_pk_f16_f32 v28, v56, v57
	ds_write_b64 v100, v[28:29] offset:57344
	s_add_u32 s70, s22, 0xc0d00
	s_addc_u32 s71, s90, 0
	global_load_dwordx4 v[28:31], v201, s[70:71] nt
	s_setprio 1
	s_waitcnt lgkmcnt(1)
	v_mfma_f32_16x16x32_f16 v[56:59], v[238:241], v[206:209], v[40:43]
	v_mfma_f32_16x16x32_f16 v[246:249], v[238:241], v[210:213], v[32:35]
	v_mfma_f32_16x16x32_f16 v[170:173], v[238:241], v[214:217], v[170:173]
	v_mfma_f32_16x16x32_f16 v[150:153], v[238:241], v[218:221], v[150:153]
	v_mfma_f32_16x16x32_f16 v[162:165], v[242:245], v[206:209], v[162:165]
	v_mfma_f32_16x16x32_f16 v[174:177], v[242:245], v[210:213], v[174:177]
	v_mfma_f32_16x16x32_f16 v[178:181], v[242:245], v[214:217], v[178:181]
	v_mfma_f32_16x16x32_f16 v[154:157], v[242:245], v[218:221], v[154:157]
	s_setprio 0
	ds_read_b128 v[40:43], v130 offset:12288
	ds_read_b128 v[238:241], v130 offset:14336
	v_cvt_pk_f16_f32 v33, v62, v63
	v_cvt_pk_f16_f32 v32, v60, v61
	ds_write_b64 v100, v[32:33] offset:61440
	s_add_u32 s70, s22, 0xe0d00
	s_addc_u32 s71, s90, 0
	global_load_dwordx4 v[32:35], v201, s[70:71] nt
	s_setprio 1
	s_waitcnt lgkmcnt(1)
	v_mfma_f32_16x16x32_f16 v[60:63], v[40:43], v[206:209], v[44:47]
	v_mfma_f32_16x16x32_f16 v[234:237], v[40:43], v[210:213], v[234:237]
	v_mfma_f32_16x16x32_f16 v[158:161], v[40:43], v[214:217], v[158:161]
	v_mfma_f32_16x16x32_f16 v[166:169], v[40:43], v[218:221], v[166:169]
	v_mfma_f32_16x16x32_f16 v[182:185], v[238:241], v[206:209], v[182:185]
	v_mfma_f32_16x16x32_f16 v[190:193], v[238:241], v[210:213], v[190:193]
	v_mfma_f32_16x16x32_f16 v[202:205], v[238:241], v[214:217], v[202:205]
	v_mfma_f32_16x16x32_f16 v[186:189], v[238:241], v[218:221], v[186:189]
	s_setprio 0
	s_waitcnt vmcnt(5)
	s_waitcnt lgkmcnt(0)
	s_barrier
	ds_read_b128 v[206:209], v131 offset:32768
	ds_read_b128 v[210:213], v131 offset:34816
	ds_read_b128 v[214:217], v131 offset:36864
	ds_read_b128 v[218:221], v131 offset:38912
	ds_read_b128 v[40:43], v129 offset:32768
	ds_read_b128 v[44:47], v129 offset:34816
	s_add_u32 s70, s22, 0xe00
	v_lshl_add_u64 v[92:93], s[50:51], 0, v[196:197]
	s_addc_u32 s71, s90, 0
	s_mov_b32 m0, s1
	v_cvt_pk_f16_f32 v11, v10, v11
	global_load_lds_dwordx4 v[92:93], off
	v_cvt_pk_f16_f32 v10, v8, v9
	ds_write_b64 v100, v[10:11]
	global_load_dwordx4 v[8:11], v201, s[70:71] nt
	s_setprio 1
	s_waitcnt lgkmcnt(1)
	v_mfma_f32_16x16x32_f16 v[104:107], v[40:43], v[214:217], v[104:107]
	v_mfma_f32_16x16x32_f16 v[108:111], v[44:47], v[206:209], v[108:111]
	v_mfma_f32_16x16x32_f16 v[112:115], v[44:47], v[210:213], v[112:115]
	v_mfma_f32_16x16x32_f16 v[116:119], v[44:47], v[214:217], v[116:119]
	v_mfma_f32_16x16x32_f16 v[238:241], v[40:43], v[206:209], v[48:51]
	v_mfma_f32_16x16x32_f16 v[230:233], v[40:43], v[210:213], v[230:233]
	v_mfma_f32_16x16x32_f16 v[222:225], v[40:43], v[218:221], v[222:225]
	v_mfma_f32_16x16x32_f16 v[226:229], v[44:47], v[218:221], v[226:229]
	s_setprio 0
	ds_read_b128 v[44:47], v129 offset:36864
	ds_read_b128 v[48:51], v129 offset:38912
	s_mov_b32 m0, s92
	v_lshl_add_u64 v[40:41], v[92:93], 0, s[58:59]
	global_load_lds_dwordx4 v[40:41], off
	v_cvt_pk_f16_f32 v41, v70, v71
	v_cvt_pk_f16_f32 v40, v68, v69
	ds_write_b64 v100, v[40:41] offset:4096
	s_add_u32 s0, s22, 0x20e00
	s_addc_u32 s1, s90, 0
	global_load_dwordx4 v[40:43], v201, s[0:1] nt
	s_setprio 1
	s_waitcnt lgkmcnt(1)
	v_mfma_f32_16x16x32_f16 v[68:71], v[44:47], v[206:209], v[52:55]
	v_mfma_f32_16x16x32_f16 v[64:67], v[44:47], v[210:213], v[64:67]
	v_mfma_f32_16x16x32_f16 v[120:123], v[44:47], v[218:221], v[120:123]
	v_mfma_f32_16x16x32_f16 v[124:127], v[48:51], v[206:209], v[124:127]
	v_mfma_f32_16x16x32_f16 v[146:149], v[48:51], v[214:217], v[146:149]
	v_mfma_f32_16x16x32_f16 v[134:137], v[48:51], v[218:221], v[134:137]
	v_mfma_f32_16x16x32_f16 v[138:141], v[44:47], v[214:217], v[138:141]
	v_mfma_f32_16x16x32_f16 v[142:145], v[48:51], v[210:213], v[142:145]
	s_setprio 0
	ds_read_b128 v[48:51], v129 offset:40960
	ds_read_b128 v[52:55], v129 offset:43008
	s_mov_b32 m0, s91
	v_lshl_add_u64 v[44:45], v[92:93], 0, s[60:61]
	global_load_lds_dwordx4 v[44:45], off
	v_cvt_pk_f16_f32 v45, v74, v75
	v_cvt_pk_f16_f32 v44, v72, v73
	ds_write_b64 v100, v[44:45] offset:8192
	s_add_u32 s0, s22, 0x40e00
	s_addc_u32 s1, s90, 0
	global_load_dwordx4 v[44:47], v201, s[0:1] nt
	s_setprio 1
	s_waitcnt lgkmcnt(1)
	v_mfma_f32_16x16x32_f16 v[72:75], v[48:51], v[206:209], v[56:59]
	v_mfma_f32_16x16x32_f16 v[242:245], v[48:51], v[210:213], v[246:249]
	v_mfma_f32_16x16x32_f16 v[170:173], v[48:51], v[214:217], v[170:173]
	v_mfma_f32_16x16x32_f16 v[150:153], v[48:51], v[218:221], v[150:153]
	v_mfma_f32_16x16x32_f16 v[162:165], v[52:55], v[206:209], v[162:165]
	v_mfma_f32_16x16x32_f16 v[174:177], v[52:55], v[210:213], v[174:177]
	v_mfma_f32_16x16x32_f16 v[178:181], v[52:55], v[214:217], v[178:181]
	v_mfma_f32_16x16x32_f16 v[154:157], v[52:55], v[218:221], v[154:157]
	s_setprio 0
	ds_read_b128 v[52:55], v129 offset:45056
	ds_read_b128 v[56:59], v129 offset:47104
	s_mov_b32 m0, s73
	v_lshl_add_u64 v[48:49], v[92:93], 0, s[62:63]
	global_load_lds_dwordx4 v[48:49], off
	v_cvt_pk_f16_f32 v49, v78, v79
	v_cvt_pk_f16_f32 v48, v76, v77
	ds_write_b64 v100, v[48:49] offset:12288
	s_add_u32 s0, s22, 0x60e00
	s_addc_u32 s1, s90, 0
	global_load_dwordx4 v[48:51], v201, s[0:1] nt
	s_setprio 1
	s_waitcnt lgkmcnt(1)
	v_mfma_f32_16x16x32_f16 v[76:79], v[52:55], v[206:209], v[60:63]
	v_mfma_f32_16x16x32_f16 v[234:237], v[52:55], v[210:213], v[234:237]
	v_mfma_f32_16x16x32_f16 v[158:161], v[52:55], v[214:217], v[158:161]
	v_mfma_f32_16x16x32_f16 v[166:169], v[52:55], v[218:221], v[166:169]
	v_mfma_f32_16x16x32_f16 v[182:185], v[56:59], v[206:209], v[182:185]
	v_mfma_f32_16x16x32_f16 v[190:193], v[56:59], v[210:213], v[190:193]
	v_mfma_f32_16x16x32_f16 v[202:205], v[56:59], v[214:217], v[202:205]
	v_mfma_f32_16x16x32_f16 v[186:189], v[56:59], v[218:221], v[186:189]
	s_setprio 0
	ds_read_b128 v[206:209], v128 offset:32768
	ds_read_b128 v[210:213], v128 offset:34816
	ds_read_b128 v[214:217], v128 offset:36864
	ds_read_b128 v[218:221], v128 offset:38912
	ds_read_b128 v[56:59], v130 offset:32768
	ds_read_b128 v[60:63], v130 offset:34816
	v_cvt_pk_f16_f32 v53, v82, v83
	v_cvt_pk_f16_f32 v52, v80, v81
	ds_write_b64 v100, v[52:53] offset:16384
	s_add_u32 s0, s22, 0x80e00
	s_addc_u32 s1, s90, 0
	global_load_dwordx4 v[52:55], v201, s[0:1] nt
	s_setprio 1
	s_waitcnt lgkmcnt(1)
	v_mfma_f32_16x16x32_f16 v[80:83], v[56:59], v[206:209], v[238:241]
	v_mfma_f32_16x16x32_f16 v[104:107], v[56:59], v[214:217], v[104:107]
	v_mfma_f32_16x16x32_f16 v[108:111], v[60:63], v[206:209], v[108:111]
	v_mfma_f32_16x16x32_f16 v[112:115], v[60:63], v[210:213], v[112:115]
	v_mfma_f32_16x16x32_f16 v[116:119], v[60:63], v[214:217], v[116:119]
	v_mfma_f32_16x16x32_f16 v[230:233], v[56:59], v[210:213], v[230:233]
	v_mfma_f32_16x16x32_f16 v[222:225], v[56:59], v[218:221], v[222:225]
	v_mfma_f32_16x16x32_f16 v[226:229], v[60:63], v[218:221], v[226:229]
	s_setprio 0
	ds_read_b128 v[60:63], v130 offset:36864
	ds_read_b128 v[238:241], v130 offset:38912
	v_cvt_pk_f16_f32 v57, v86, v87
	v_cvt_pk_f16_f32 v56, v84, v85
	ds_write_b64 v100, v[56:57] offset:20480
	s_add_u32 s0, s22, 0xa0e00
	s_addc_u32 s1, s90, 0
	global_load_dwordx4 v[56:59], v201, s[0:1] nt
	s_setprio 1
	s_waitcnt lgkmcnt(1)
	v_mfma_f32_16x16x32_f16 v[68:71], v[60:63], v[206:209], v[68:71]
	v_mfma_f32_16x16x32_f16 v[64:67], v[60:63], v[210:213], v[64:67]
	v_mfma_f32_16x16x32_f16 v[84:87], v[60:63], v[214:217], v[138:141]
	v_mfma_f32_16x16x32_f16 v[120:123], v[60:63], v[218:221], v[120:123]
	v_mfma_f32_16x16x32_f16 v[124:127], v[238:241], v[206:209], v[124:127]
	v_mfma_f32_16x16x32_f16 v[134:137], v[238:241], v[218:221], v[134:137]
	v_mfma_f32_16x16x32_f16 v[138:141], v[238:241], v[210:213], v[142:145]
	v_mfma_f32_16x16x32_f16 v[142:145], v[238:241], v[214:217], v[146:149]
	s_setprio 0
	s_nop 1
	ds_read_b128 v[146:149], v130 offset:40960
	ds_read_b128 v[238:241], v130 offset:43008
	v_cvt_pk_f16_f32 v61, v90, v91
	v_cvt_pk_f16_f32 v60, v88, v89
	ds_write_b64 v100, v[60:61] offset:24576
	s_add_u32 s0, s22, 0xc0e00
	s_addc_u32 s1, s90, 0
	global_load_dwordx4 v[60:63], v201, s[0:1] nt
	s_setprio 1
	s_waitcnt lgkmcnt(1)
	v_mfma_f32_16x16x32_f16 v[72:75], v[146:149], v[206:209], v[72:75]
	v_mfma_f32_16x16x32_f16 v[88:91], v[146:149], v[210:213], v[242:245]
	v_mfma_f32_16x16x32_f16 v[170:173], v[146:149], v[214:217], v[170:173]
	v_mfma_f32_16x16x32_f16 v[146:149], v[146:149], v[218:221], v[150:153]
	v_mfma_f32_16x16x32_f16 v[150:153], v[238:241], v[206:209], v[162:165]
	v_mfma_f32_16x16x32_f16 v[162:165], v[238:241], v[210:213], v[174:177]
	v_mfma_f32_16x16x32_f16 v[174:177], v[238:241], v[214:217], v[178:181]
	v_mfma_f32_16x16x32_f16 v[154:157], v[238:241], v[218:221], v[154:157]
	s_setprio 0
	s_nop 0
	ds_read_b128 v[178:181], v130 offset:45056
	ds_read_b128 v[238:241], v130 offset:47104
	v_cvt_pk_f16_f32 v39, v38, v39
	v_cvt_pk_f16_f32 v38, v36, v37
	ds_write_b64 v100, v[38:39] offset:28672
	s_add_u32 s0, s22, 0xe0e00
	s_addc_u32 s1, s90, 0
	global_load_dwordx4 v[36:39], v201, s[0:1] nt
	s_setprio 1
	s_waitcnt lgkmcnt(1)
	v_mfma_f32_16x16x32_f16 v[76:79], v[178:181], v[206:209], v[76:79]
	v_mfma_f32_16x16x32_f16 v[234:237], v[178:181], v[210:213], v[234:237]
	v_mfma_f32_16x16x32_f16 v[158:161], v[178:181], v[214:217], v[158:161]
	v_mfma_f32_16x16x32_f16 v[166:169], v[178:181], v[218:221], v[166:169]
	v_mfma_f32_16x16x32_f16 v[178:181], v[238:241], v[206:209], v[182:185]
	v_mfma_f32_16x16x32_f16 v[182:185], v[238:241], v[210:213], v[190:193]
	v_mfma_f32_16x16x32_f16 v[190:193], v[238:241], v[214:217], v[202:205]
	v_mfma_f32_16x16x32_f16 v[186:189], v[238:241], v[218:221], v[186:189]
	s_setprio 0
	s_waitcnt vmcnt(5)
	s_waitcnt lgkmcnt(0)
	s_barrier
	ds_read_b128 v[202:205], v131
	ds_read_b128 v[206:209], v131 offset:2048
	ds_read_b128 v[210:213], v131 offset:4096
	ds_read_b128 v[214:217], v131 offset:6144
	ds_read_b128 v[218:221], v129
	ds_read_b128 v[238:241], v129 offset:2048
	s_add_u32 s70, s22, 0xf00
	v_lshl_add_u64 v[92:93], s[52:53], 0, v[196:197]
	s_addc_u32 s71, s90, 0
	v_readfirstlane_b32 s0, v95
	s_mov_b32 m0, s0
	v_cvt_pk_f16_f32 v3, v2, v3
	global_load_lds_dwordx4 v[92:93], off
	v_cvt_pk_f16_f32 v2, v0, v1
	ds_write_b64 v100, v[2:3] offset:32768
	global_load_dwordx4 v[0:3], v201, s[70:71] nt
	s_setprio 1
	s_waitcnt lgkmcnt(1)
	v_mfma_f32_16x16x32_f16 v[80:83], v[218:221], v[202:205], v[80:83]
	v_mfma_f32_16x16x32_f16 v[104:107], v[218:221], v[210:213], v[104:107]
	v_mfma_f32_16x16x32_f16 v[108:111], v[238:241], v[202:205], v[108:111]
	v_mfma_f32_16x16x32_f16 v[112:115], v[238:241], v[206:209], v[112:115]
	v_mfma_f32_16x16x32_f16 v[116:119], v[238:241], v[210:213], v[116:119]
	v_mfma_f32_16x16x32_f16 v[230:233], v[218:221], v[206:209], v[230:233]
	v_mfma_f32_16x16x32_f16 v[218:221], v[218:221], v[214:217], v[222:225]
	v_mfma_f32_16x16x32_f16 v[222:225], v[238:241], v[214:217], v[226:229]
	s_setprio 0
	s_nop 1
	ds_read_b128 v[226:229], v129 offset:4096
	ds_read_b128 v[238:241], v129 offset:6144
	v_readfirstlane_b32 s1, v96
	v_lshl_add_u64 v[198:199], v[92:93], 0, s[58:59]
	s_mov_b32 m0, s1
	v_cvt_pk_f16_f32 v7, v6, v7
	global_load_lds_dwordx4 v[198:199], off
	v_cvt_pk_f16_f32 v6, v4, v5
	ds_write_b64 v100, v[6:7] offset:36864
	s_add_u32 s70, s22, 0x20f00
	s_addc_u32 s71, s90, 0
	global_load_dwordx4 v[4:7], v201, s[70:71] nt
	s_setprio 1
	s_waitcnt lgkmcnt(1)
	v_mfma_f32_16x16x32_f16 v[68:71], v[226:229], v[202:205], v[68:71]
	v_mfma_f32_16x16x32_f16 v[64:67], v[226:229], v[206:209], v[64:67]
	v_mfma_f32_16x16x32_f16 v[84:87], v[226:229], v[210:213], v[84:87]
	v_mfma_f32_16x16x32_f16 v[120:123], v[226:229], v[214:217], v[120:123]
	v_mfma_f32_16x16x32_f16 v[124:127], v[238:241], v[202:205], v[124:127]
	v_mfma_f32_16x16x32_f16 v[134:137], v[238:241], v[214:217], v[134:137]
	v_mfma_f32_16x16x32_f16 v[138:141], v[238:241], v[206:209], v[138:141]
	v_mfma_f32_16x16x32_f16 v[142:145], v[238:241], v[210:213], v[142:145]
	s_setprio 0
	ds_read_b128 v[226:229], v129 offset:8192
	ds_read_b128 v[238:241], v129 offset:10240
	v_readfirstlane_b32 s70, v97
	v_lshl_add_u64 v[198:199], v[92:93], 0, s[60:61]
	s_mov_b32 m0, s70
	v_cvt_pk_f16_f32 v15, v14, v15
	global_load_lds_dwordx4 v[198:199], off
	v_cvt_pk_f16_f32 v14, v12, v13
	ds_write_b64 v100, v[14:15] offset:40960
	s_add_u32 s72, s22, 0x40f00
	s_addc_u32 s73, s90, 0
	global_load_dwordx4 v[12:15], v201, s[72:73] nt
	s_setprio 1
	s_waitcnt lgkmcnt(1)
	v_mfma_f32_16x16x32_f16 v[72:75], v[226:229], v[202:205], v[72:75]
	v_mfma_f32_16x16x32_f16 v[88:91], v[226:229], v[206:209], v[88:91]
	v_mfma_f32_16x16x32_f16 v[146:149], v[226:229], v[214:217], v[146:149]
	v_mfma_f32_16x16x32_f16 v[170:173], v[226:229], v[210:213], v[170:173]
	v_mfma_f32_16x16x32_f16 v[150:153], v[238:241], v[202:205], v[150:153]
	v_mfma_f32_16x16x32_f16 v[162:165], v[238:241], v[206:209], v[162:165]
	v_mfma_f32_16x16x32_f16 v[174:177], v[238:241], v[210:213], v[174:177]
	v_mfma_f32_16x16x32_f16 v[154:157], v[238:241], v[214:217], v[154:157]
	s_setprio 0
	ds_read_b128 v[226:229], v129 offset:12288
	ds_read_b128 v[238:241], v129 offset:14336
	v_readfirstlane_b32 s71, v98
	v_lshl_add_u64 v[92:93], v[92:93], 0, s[62:63]
	s_mov_b32 m0, s71
	v_cvt_pk_f16_f32 v19, v18, v19
	global_load_lds_dwordx4 v[92:93], off
	v_cvt_pk_f16_f32 v18, v16, v17
	ds_write_b64 v100, v[18:19] offset:45056
	s_add_u32 s72, s22, 0x60f00
	s_addc_u32 s73, s90, 0
	global_load_dwordx4 v[16:19], v201, s[72:73] nt
	s_setprio 1
	s_waitcnt lgkmcnt(1)
	v_mfma_f32_16x16x32_f16 v[76:79], v[226:229], v[202:205], v[76:79]
	v_mfma_f32_16x16x32_f16 v[234:237], v[226:229], v[206:209], v[234:237]
	v_mfma_f32_16x16x32_f16 v[158:161], v[226:229], v[210:213], v[158:161]
	v_mfma_f32_16x16x32_f16 v[166:169], v[226:229], v[214:217], v[166:169]
	v_mfma_f32_16x16x32_f16 v[178:181], v[238:241], v[202:205], v[178:181]
	v_mfma_f32_16x16x32_f16 v[182:185], v[238:241], v[206:209], v[182:185]
	v_mfma_f32_16x16x32_f16 v[190:193], v[238:241], v[210:213], v[190:193]
	v_mfma_f32_16x16x32_f16 v[186:189], v[238:241], v[214:217], v[186:189]
	s_setprio 0
	ds_read_b128 v[202:205], v128
	ds_read_b128 v[206:209], v128 offset:2048
	ds_read_b128 v[210:213], v128 offset:4096
	ds_read_b128 v[214:217], v128 offset:6144
	ds_read_b128 v[226:229], v130
	ds_read_b128 v[238:241], v130 offset:2048
	v_cvt_pk_f16_f32 v23, v22, v23
	v_cvt_pk_f16_f32 v22, v20, v21
	ds_write_b64 v100, v[22:23] offset:49152
	s_add_u32 s72, s22, 0x80f00
	s_addc_u32 s73, s90, 0
	global_load_dwordx4 v[20:23], v201, s[72:73] nt
	s_setprio 1
	s_waitcnt lgkmcnt(1)
	v_mfma_f32_16x16x32_f16 v[80:83], v[226:229], v[202:205], v[80:83]
	v_mfma_f32_16x16x32_f16 v[104:107], v[226:229], v[210:213], v[104:107]
	v_mfma_f32_16x16x32_f16 v[108:111], v[238:241], v[202:205], v[108:111]
	v_mfma_f32_16x16x32_f16 v[112:115], v[238:241], v[206:209], v[112:115]
	v_mfma_f32_16x16x32_f16 v[116:119], v[238:241], v[210:213], v[116:119]
	v_mfma_f32_16x16x32_f16 v[230:233], v[226:229], v[206:209], v[230:233]
	v_mfma_f32_16x16x32_f16 v[218:221], v[226:229], v[214:217], v[218:221]
	v_mfma_f32_16x16x32_f16 v[222:225], v[238:241], v[214:217], v[222:225]
	s_setprio 0
	ds_read_b128 v[226:229], v130 offset:4096
	ds_read_b128 v[238:241], v130 offset:6144
	v_cvt_pk_f16_f32 v27, v26, v27
	v_cvt_pk_f16_f32 v26, v24, v25
	ds_write_b64 v100, v[26:27] offset:53248
	s_add_u32 s72, s22, 0xa0f00
	s_addc_u32 s73, s90, 0
	global_load_dwordx4 v[24:27], v201, s[72:73] nt
	s_setprio 1
	s_waitcnt lgkmcnt(1)
	v_mfma_f32_16x16x32_f16 v[68:71], v[226:229], v[202:205], v[68:71]
	v_mfma_f32_16x16x32_f16 v[64:67], v[226:229], v[206:209], v[64:67]
	v_mfma_f32_16x16x32_f16 v[84:87], v[226:229], v[210:213], v[84:87]
	v_mfma_f32_16x16x32_f16 v[120:123], v[226:229], v[214:217], v[120:123]
	v_mfma_f32_16x16x32_f16 v[124:127], v[238:241], v[202:205], v[124:127]
	v_mfma_f32_16x16x32_f16 v[134:137], v[238:241], v[214:217], v[134:137]
	v_mfma_f32_16x16x32_f16 v[138:141], v[238:241], v[206:209], v[138:141]
	v_mfma_f32_16x16x32_f16 v[142:145], v[238:241], v[210:213], v[142:145]
	s_setprio 0
	ds_read_b128 v[226:229], v130 offset:8192
	ds_read_b128 v[238:241], v130 offset:10240
	v_cvt_pk_f16_f32 v31, v30, v31
	v_cvt_pk_f16_f32 v30, v28, v29
	ds_write_b64 v100, v[30:31] offset:57344
	s_add_u32 s72, s22, 0xc0f00
	s_addc_u32 s73, s90, 0
	global_load_dwordx4 v[28:31], v201, s[72:73] nt
	s_setprio 1
	s_waitcnt lgkmcnt(1)
	v_mfma_f32_16x16x32_f16 v[72:75], v[226:229], v[202:205], v[72:75]
	v_mfma_f32_16x16x32_f16 v[88:91], v[226:229], v[206:209], v[88:91]
	v_mfma_f32_16x16x32_f16 v[146:149], v[226:229], v[214:217], v[146:149]
	v_mfma_f32_16x16x32_f16 v[170:173], v[226:229], v[210:213], v[170:173]
	v_mfma_f32_16x16x32_f16 v[150:153], v[238:241], v[202:205], v[150:153]
	v_mfma_f32_16x16x32_f16 v[162:165], v[238:241], v[206:209], v[162:165]
	v_mfma_f32_16x16x32_f16 v[174:177], v[238:241], v[210:213], v[174:177]
	v_mfma_f32_16x16x32_f16 v[154:157], v[238:241], v[214:217], v[154:157]
	s_setprio 0
	ds_read_b128 v[226:229], v130 offset:12288
	ds_read_b128 v[238:241], v130 offset:14336
	v_cvt_pk_f16_f32 v35, v34, v35
	v_cvt_pk_f16_f32 v34, v32, v33
	ds_write_b64 v100, v[34:35] offset:61440
	s_add_u32 s72, s22, 0xe0f00
	s_addc_u32 s73, s90, 0
	global_load_dwordx4 v[32:35], v201, s[72:73] nt
	s_setprio 1
	s_waitcnt lgkmcnt(1)
	v_mfma_f32_16x16x32_f16 v[76:79], v[226:229], v[202:205], v[76:79]
	v_mfma_f32_16x16x32_f16 v[234:237], v[226:229], v[206:209], v[234:237]
	v_mfma_f32_16x16x32_f16 v[158:161], v[226:229], v[210:213], v[158:161]
	v_mfma_f32_16x16x32_f16 v[166:169], v[226:229], v[214:217], v[166:169]
	v_mfma_f32_16x16x32_f16 v[178:181], v[238:241], v[202:205], v[178:181]
	v_mfma_f32_16x16x32_f16 v[182:185], v[238:241], v[206:209], v[182:185]
	v_mfma_f32_16x16x32_f16 v[190:193], v[238:241], v[210:213], v[190:193]
	v_mfma_f32_16x16x32_f16 v[186:189], v[238:241], v[214:217], v[186:189]
	s_setprio 0
	s_waitcnt vmcnt(5)
	s_waitcnt lgkmcnt(0)
	s_barrier
	ds_read_b128 v[202:205], v131 offset:32768
	ds_read_b128 v[206:209], v131 offset:34816
	ds_read_b128 v[210:213], v131 offset:36864
	ds_read_b128 v[214:217], v131 offset:38912
	ds_read_b128 v[226:229], v129 offset:32768
	ds_read_b128 v[238:241], v129 offset:34816
	v_lshl_add_u64 v[198:199], s[54:55], 0, v[196:197]
	v_readfirstlane_b32 s64, v94
	s_mov_b32 m0, s64
	v_cvt_pk_f16_f32 v11, v10, v11
	global_load_lds_dwordx4 v[198:199], off
	v_cvt_pk_f16_f32 v10, v8, v9
	ds_write_b64 v100, v[10:11]
	s_setprio 1
	s_waitcnt lgkmcnt(1)
	v_mfma_f32_16x16x32_f16 v[8:11], v[226:229], v[202:205], v[80:83]
	v_mfma_f32_16x16x32_f16 v[80:83], v[226:229], v[206:209], v[230:233]
	v_mfma_f32_16x16x32_f16 v[92:95], v[226:229], v[210:213], v[104:107]
	v_mfma_f32_16x16x32_f16 v[104:107], v[226:229], v[214:217], v[218:221]
	v_mfma_f32_16x16x32_f16 v[108:111], v[238:241], v[202:205], v[108:111]
	v_mfma_f32_16x16x32_f16 v[112:115], v[238:241], v[206:209], v[112:115]
	v_mfma_f32_16x16x32_f16 v[116:119], v[238:241], v[210:213], v[116:119]
	v_mfma_f32_16x16x32_f16 v[218:221], v[238:241], v[214:217], v[222:225]
	s_setprio 0
	s_nop 1
	ds_read_b128 v[222:225], v129 offset:36864
	ds_read_b128 v[226:229], v129 offset:38912
	v_readfirstlane_b32 s64, v99
	v_lshl_add_u64 v[96:97], v[198:199], 0, s[58:59]
	s_mov_b32 m0, s64
	v_cvt_pk_f16_f32 v43, v42, v43
	global_load_lds_dwordx4 v[96:97], off
	v_cvt_pk_f16_f32 v42, v40, v41
	ds_write_b64 v100, v[42:43] offset:4096
	s_setprio 1
	s_waitcnt lgkmcnt(1)
	v_mfma_f32_16x16x32_f16 v[40:43], v[222:225], v[202:205], v[68:71]
	v_mfma_f32_16x16x32_f16 v[64:67], v[222:225], v[206:209], v[64:67]
	v_mfma_f32_16x16x32_f16 v[68:71], v[222:225], v[210:213], v[84:87]
	v_mfma_f32_16x16x32_f16 v[84:87], v[222:225], v[214:217], v[120:123]
	v_mfma_f32_16x16x32_f16 v[96:99], v[226:229], v[202:205], v[124:127]
	v_mfma_f32_16x16x32_f16 v[120:123], v[226:229], v[206:209], v[138:141]
	v_mfma_f32_16x16x32_f16 v[124:127], v[226:229], v[210:213], v[142:145]
	v_mfma_f32_16x16x32_f16 v[134:137], v[226:229], v[214:217], v[134:137]
	s_setprio 0
	ds_read_b128 v[138:141], v129 offset:40960
	ds_read_b128 v[142:145], v129 offset:43008
	v_readfirstlane_b32 s64, v101
	v_lshl_add_u64 v[222:223], v[198:199], 0, s[60:61]
	s_mov_b32 m0, s64
	v_cvt_pk_f16_f32 v47, v46, v47
	global_load_lds_dwordx4 v[222:223], off
	v_cvt_pk_f16_f32 v46, v44, v45
	ds_write_b64 v100, v[46:47] offset:8192
	s_setprio 1
	s_waitcnt lgkmcnt(1)
	v_mfma_f32_16x16x32_f16 v[44:47], v[138:141], v[202:205], v[72:75]
	v_mfma_f32_16x16x32_f16 v[72:75], v[138:141], v[206:209], v[88:91]
	v_mfma_f32_16x16x32_f16 v[88:91], v[138:141], v[210:213], v[170:173]
	v_mfma_f32_16x16x32_f16 v[138:141], v[138:141], v[214:217], v[146:149]
	v_mfma_f32_16x16x32_f16 v[146:149], v[142:145], v[202:205], v[150:153]
	v_mfma_f32_16x16x32_f16 v[150:153], v[142:145], v[206:209], v[162:165]
	v_mfma_f32_16x16x32_f16 v[162:165], v[142:145], v[210:213], v[174:177]
	v_mfma_f32_16x16x32_f16 v[142:145], v[142:145], v[214:217], v[154:157]
	s_setprio 0
	s_nop 1
	ds_read_b128 v[154:157], v129 offset:45056
	ds_read_b128 v[170:173], v129 offset:47104
	v_readfirstlane_b32 s64, v102
	v_lshl_add_u64 v[174:175], v[198:199], 0, s[62:63]
	s_mov_b32 m0, s64
	v_cvt_pk_f16_f32 v51, v50, v51
	global_load_lds_dwordx4 v[174:175], off
	v_cvt_pk_f16_f32 v50, v48, v49
	ds_write_b64 v100, v[50:51] offset:12288
	s_setprio 1
	s_waitcnt lgkmcnt(1)
	v_mfma_f32_16x16x32_f16 v[48:51], v[154:157], v[202:205], v[76:79]
	v_mfma_f32_16x16x32_f16 v[76:79], v[154:157], v[206:209], v[234:237]
	v_mfma_f32_16x16x32_f16 v[158:161], v[154:157], v[210:213], v[158:161]
	v_mfma_f32_16x16x32_f16 v[154:157], v[154:157], v[214:217], v[166:169]
	v_mfma_f32_16x16x32_f16 v[166:169], v[170:173], v[202:205], v[178:181]
	v_mfma_f32_16x16x32_f16 v[174:177], v[170:173], v[206:209], v[182:185]
	v_mfma_f32_16x16x32_f16 v[178:181], v[170:173], v[210:213], v[190:193]
	v_mfma_f32_16x16x32_f16 v[170:173], v[170:173], v[214:217], v[186:189]
	s_setprio 0
	ds_read_b128 v[182:185], v128 offset:32768
	s_nop 0
	ds_read_b128 v[186:189], v128 offset:34816
	ds_read_b128 v[190:193], v128 offset:36864
	ds_read_b128 v[202:205], v128 offset:38912
	ds_read_b128 v[206:209], v130 offset:32768
	ds_read_b128 v[210:213], v130 offset:34816
	v_cvt_pk_f16_f32 v55, v54, v55
	v_cvt_pk_f16_f32 v54, v52, v53
	ds_write_b64 v100, v[54:55] offset:16384
	s_setprio 1
	s_waitcnt lgkmcnt(1)
	v_mfma_f32_16x16x32_f16 v[8:11], v[206:209], v[182:185], v[8:11]
	v_mfma_f32_16x16x32_f16 v[52:55], v[206:209], v[186:189], v[80:83]
	v_mfma_f32_16x16x32_f16 v[80:83], v[206:209], v[190:193], v[92:95]
	v_mfma_f32_16x16x32_f16 v[92:95], v[206:209], v[202:205], v[104:107]
	v_mfma_f32_16x16x32_f16 v[102:105], v[210:213], v[182:185], v[108:111]
	v_mfma_f32_16x16x32_f16 v[106:109], v[210:213], v[186:189], v[112:115]
	v_mfma_f32_16x16x32_f16 v[110:113], v[210:213], v[190:193], v[116:119]
	v_mfma_f32_16x16x32_f16 v[114:117], v[210:213], v[202:205], v[218:221]
	s_setprio 0
	ds_read_b128 v[206:209], v130 offset:36864
	ds_read_b128 v[210:213], v130 offset:38912
	v_cvt_pk_f16_f32 v59, v58, v59
	v_cvt_pk_f16_f32 v58, v56, v57
	ds_write_b64 v100, v[58:59] offset:20480
	s_setprio 1
	s_waitcnt lgkmcnt(1)
	v_mfma_f32_16x16x32_f16 v[40:43], v[206:209], v[182:185], v[40:43]
	v_mfma_f32_16x16x32_f16 v[56:59], v[206:209], v[186:189], v[64:67]
	v_mfma_f32_16x16x32_f16 v[64:67], v[206:209], v[190:193], v[68:71]
	v_mfma_f32_16x16x32_f16 v[68:71], v[206:209], v[202:205], v[84:87]
	v_mfma_f32_16x16x32_f16 v[84:87], v[210:213], v[182:185], v[96:99]
	v_mfma_f32_16x16x32_f16 v[96:99], v[210:213], v[186:189], v[120:123]
	v_mfma_f32_16x16x32_f16 v[118:121], v[210:213], v[190:193], v[124:127]
	v_mfma_f32_16x16x32_f16 v[122:125], v[210:213], v[202:205], v[134:137]
	s_setprio 0
	s_nop 1
	ds_read_b128 v[134:137], v130 offset:40960
	ds_read_b128 v[206:209], v130 offset:43008
	v_cvt_pk_f16_f32 v63, v62, v63
	v_cvt_pk_f16_f32 v62, v60, v61
	ds_write_b64 v100, v[62:63] offset:24576
	s_setprio 1
	s_waitcnt lgkmcnt(1)
	v_mfma_f32_16x16x32_f16 v[44:47], v[134:137], v[182:185], v[44:47]
	v_mfma_f32_16x16x32_f16 v[60:63], v[134:137], v[186:189], v[72:75]
	v_mfma_f32_16x16x32_f16 v[72:75], v[134:137], v[190:193], v[88:91]
	v_mfma_f32_16x16x32_f16 v[88:91], v[134:137], v[202:205], v[138:141]
	v_mfma_f32_16x16x32_f16 v[134:137], v[206:209], v[182:185], v[146:149]
	v_mfma_f32_16x16x32_f16 v[146:149], v[206:209], v[190:193], v[162:165]
	v_mfma_f32_16x16x32_f16 v[138:141], v[206:209], v[186:189], v[150:153]
	v_mfma_f32_16x16x32_f16 v[142:145], v[206:209], v[202:205], v[142:145]
	s_setprio 0
	s_nop 0
	ds_read_b128 v[150:153], v130 offset:45056
	ds_read_b128 v[162:165], v130 offset:47104
	v_cvt_pk_f16_f32 v39, v38, v39
	v_cvt_pk_f16_f32 v38, v36, v37
	ds_write_b64 v100, v[38:39] offset:28672
	s_setprio 1
	s_waitcnt lgkmcnt(1)
	v_mfma_f32_16x16x32_f16 v[36:39], v[150:153], v[182:185], v[48:51]
	v_mfma_f32_16x16x32_f16 v[48:51], v[150:153], v[186:189], v[76:79]
	v_mfma_f32_16x16x32_f16 v[76:79], v[150:153], v[190:193], v[158:161]
	v_mfma_f32_16x16x32_f16 v[150:153], v[150:153], v[202:205], v[154:157]
	v_mfma_f32_16x16x32_f16 v[154:157], v[162:165], v[182:185], v[166:169]
	v_mfma_f32_16x16x32_f16 v[158:161], v[162:165], v[186:189], v[174:177]
	v_mfma_f32_16x16x32_f16 v[166:169], v[162:165], v[190:193], v[178:181]
	v_mfma_f32_16x16x32_f16 v[162:165], v[162:165], v[202:205], v[170:173]
	s_setprio 0
	s_waitcnt vmcnt(0)
	s_waitcnt lgkmcnt(0)
	s_barrier
	s_nop 0
	ds_read_b128 v[170:173], v131
	ds_read_b128 v[174:177], v131 offset:2048
	ds_read_b128 v[178:181], v131 offset:4096
	ds_read_b128 v[182:185], v131 offset:6144
	ds_read_b128 v[186:189], v129
	ds_read_b128 v[190:193], v129 offset:2048
	v_lshl_add_u64 v[126:127], s[56:57], 0, v[196:197]
	s_mov_b32 m0, s0
	v_cvt_pk_f16_f32 v3, v2, v3
	global_load_lds_dwordx4 v[126:127], off
	v_cvt_pk_f16_f32 v2, v0, v1
	ds_write_b64 v100, v[2:3] offset:32768
	s_setprio 1
	s_waitcnt lgkmcnt(1)
	v_mfma_f32_16x16x32_f16 v[0:3], v[186:189], v[170:173], v[8:11]
	v_mfma_f32_16x16x32_f16 v[8:11], v[186:189], v[174:177], v[52:55]
	v_mfma_f32_16x16x32_f16 v[52:55], v[186:189], v[178:181], v[80:83]
	v_mfma_f32_16x16x32_f16 v[80:83], v[186:189], v[182:185], v[92:95]
	v_mfma_f32_16x16x32_f16 v[92:95], v[190:193], v[170:173], v[102:105]
	v_mfma_f32_16x16x32_f16 v[102:105], v[190:193], v[174:177], v[106:109]
	v_mfma_f32_16x16x32_f16 v[106:109], v[190:193], v[178:181], v[110:113]
	v_mfma_f32_16x16x32_f16 v[110:113], v[190:193], v[182:185], v[114:117]
	s_setprio 0
	s_nop 1
	ds_read_b128 v[114:117], v129 offset:4096
	ds_read_b128 v[186:189], v129 offset:6144
	s_mov_b32 m0, s1
	v_lshl_add_u64 v[190:191], v[126:127], 0, s[58:59]
	global_load_lds_dwordx4 v[190:191], off
	v_cvt_pk_f16_f32 v7, v6, v7
	v_cvt_pk_f16_f32 v6, v4, v5
	ds_write_b64 v100, v[6:7] offset:36864
	s_setprio 1
	s_waitcnt lgkmcnt(1)
	v_mfma_f32_16x16x32_f16 v[190:193], v[114:117], v[170:173], v[40:43]
	v_mfma_f32_16x16x32_f16 v[56:59], v[114:117], v[174:177], v[56:59]
	v_mfma_f32_16x16x32_f16 v[64:67], v[114:117], v[178:181], v[64:67]
	v_mfma_f32_16x16x32_f16 v[68:71], v[114:117], v[182:185], v[68:71]
	v_mfma_f32_16x16x32_f16 v[84:87], v[186:189], v[170:173], v[84:87]
	v_mfma_f32_16x16x32_f16 v[96:99], v[186:189], v[174:177], v[96:99]
	v_mfma_f32_16x16x32_f16 v[114:117], v[186:189], v[178:181], v[118:121]
	v_mfma_f32_16x16x32_f16 v[118:121], v[186:189], v[182:185], v[122:125]
	s_setprio 0
	ds_read_b128 v[4:7], v129 offset:8192
	ds_read_b128 v[40:43], v129 offset:10240
	s_mov_b32 m0, s70
	v_lshl_add_u64 v[122:123], v[126:127], 0, s[60:61]
	global_load_lds_dwordx4 v[122:123], off
	v_cvt_pk_f16_f32 v15, v14, v15
	v_cvt_pk_f16_f32 v14, v12, v13
	ds_write_b64 v100, v[14:15] offset:40960
	s_setprio 1
	s_waitcnt lgkmcnt(1)
	v_mfma_f32_16x16x32_f16 v[122:125], v[4:7], v[170:173], v[44:47]
	v_mfma_f32_16x16x32_f16 v[88:91], v[4:7], v[182:185], v[88:91]
	v_mfma_f32_16x16x32_f16 v[134:137], v[40:43], v[170:173], v[134:137]
	v_mfma_f32_16x16x32_f16 v[146:149], v[40:43], v[178:181], v[146:149]
	v_mfma_f32_16x16x32_f16 v[186:189], v[4:7], v[174:177], v[60:63]
	v_mfma_f32_16x16x32_f16 v[202:205], v[4:7], v[178:181], v[72:75]
	v_mfma_f32_16x16x32_f16 v[138:141], v[40:43], v[174:177], v[138:141]
	v_mfma_f32_16x16x32_f16 v[142:145], v[40:43], v[182:185], v[142:145]
	s_setprio 0
	ds_read_b128 v[4:7], v129 offset:12288
	ds_read_b128 v[12:15], v129 offset:14336
	s_mov_b32 m0, s71
	v_lshl_add_u64 v[40:41], v[126:127], 0, s[62:63]
	global_load_lds_dwordx4 v[40:41], off
	v_cvt_pk_f16_f32 v19, v18, v19
	v_cvt_pk_f16_f32 v18, v16, v17
	ds_write_b64 v100, v[18:19] offset:45056
	s_setprio 1
	s_waitcnt lgkmcnt(1)
	v_mfma_f32_16x16x32_f16 v[206:209], v[4:7], v[170:173], v[36:39]
	v_mfma_f32_16x16x32_f16 v[210:213], v[4:7], v[174:177], v[48:51]
	v_mfma_f32_16x16x32_f16 v[214:217], v[4:7], v[178:181], v[76:79]
	v_mfma_f32_16x16x32_f16 v[150:153], v[4:7], v[182:185], v[150:153]
	v_mfma_f32_16x16x32_f16 v[154:157], v[12:15], v[170:173], v[154:157]
	v_mfma_f32_16x16x32_f16 v[158:161], v[12:15], v[174:177], v[158:161]
	v_mfma_f32_16x16x32_f16 v[166:169], v[12:15], v[178:181], v[166:169]
	v_mfma_f32_16x16x32_f16 v[162:165], v[12:15], v[182:185], v[162:165]
	s_setprio 0
	ds_read_b128 v[170:173], v128
	ds_read_b128 v[174:177], v128 offset:2048
	ds_read_b128 v[178:181], v128 offset:4096
	ds_read_b128 v[182:185], v128 offset:6144
	ds_read_b128 v[12:15], v130
	ds_read_b128 v[40:43], v130 offset:2048
	v_cvt_pk_f16_f32 v5, v22, v23
	v_cvt_pk_f16_f32 v4, v20, v21
	ds_write_b64 v100, v[4:5] offset:49152
	s_setprio 1
	s_waitcnt lgkmcnt(1)
	v_mfma_f32_16x16x32_f16 v[0:3], v[12:15], v[170:173], v[0:3]
	v_mfma_f32_16x16x32_f16 v[4:7], v[12:15], v[174:177], v[8:11]
	v_mfma_f32_16x16x32_f16 v[8:11], v[12:15], v[178:181], v[52:55]
	v_mfma_f32_16x16x32_f16 v[12:15], v[12:15], v[182:185], v[80:83]
	v_mfma_f32_16x16x32_f16 v[16:19], v[40:43], v[170:173], v[92:95]
	v_mfma_f32_16x16x32_f16 v[20:23], v[40:43], v[174:177], v[102:105]
	v_mfma_f32_16x16x32_f16 v[36:39], v[40:43], v[178:181], v[106:109]
	v_mfma_f32_16x16x32_f16 v[40:43], v[40:43], v[182:185], v[110:113]
	s_setprio 0
	ds_read_b128 v[52:55], v130 offset:4096
	ds_read_b128 v[72:75], v130 offset:6144
	v_cvt_pk_f16_f32 v27, v26, v27
	v_cvt_pk_f16_f32 v26, v24, v25
	ds_write_b64 v100, v[26:27] offset:53248
	s_setprio 1
	s_waitcnt lgkmcnt(1)
	v_mfma_f32_16x16x32_f16 v[24:27], v[52:55], v[170:173], v[190:193]
	v_mfma_f32_16x16x32_f16 v[44:47], v[52:55], v[174:177], v[56:59]
	v_mfma_f32_16x16x32_f16 v[48:51], v[52:55], v[178:181], v[64:67]
	v_mfma_f32_16x16x32_f16 v[52:55], v[52:55], v[182:185], v[68:71]
	v_mfma_f32_16x16x32_f16 v[56:59], v[72:75], v[170:173], v[84:87]
	v_mfma_f32_16x16x32_f16 v[60:63], v[72:75], v[174:177], v[96:99]
	v_mfma_f32_16x16x32_f16 v[64:67], v[72:75], v[178:181], v[114:117]
	v_mfma_f32_16x16x32_f16 v[68:71], v[72:75], v[182:185], v[118:121]
	s_setprio 0
	ds_read_b128 v[80:83], v130 offset:8192
	ds_read_b128 v[96:99], v130 offset:10240
	v_cvt_pk_f16_f32 v31, v30, v31
	v_cvt_pk_f16_f32 v30, v28, v29
	ds_write_b64 v100, v[30:31] offset:57344
	s_setprio 1
	s_waitcnt lgkmcnt(1)
	v_mfma_f32_16x16x32_f16 v[28:31], v[80:83], v[170:173], v[122:125]
	v_mfma_f32_16x16x32_f16 v[72:75], v[80:83], v[174:177], v[186:189]
	v_mfma_f32_16x16x32_f16 v[76:79], v[80:83], v[178:181], v[202:205]
	v_mfma_f32_16x16x32_f16 v[80:83], v[80:83], v[182:185], v[88:91]
	v_mfma_f32_16x16x32_f16 v[84:87], v[96:99], v[170:173], v[134:137]
	v_mfma_f32_16x16x32_f16 v[88:91], v[96:99], v[174:177], v[138:141]
	v_mfma_f32_16x16x32_f16 v[92:95], v[96:99], v[178:181], v[146:149]
	v_mfma_f32_16x16x32_f16 v[96:99], v[96:99], v[182:185], v[142:145]
	s_setprio 0
	ds_read_b128 v[108:111], v130 offset:12288
	ds_read_b128 v[124:127], v130 offset:14336
	v_cvt_pk_f16_f32 v35, v34, v35
	v_cvt_pk_f16_f32 v34, v32, v33
	ds_write_b64 v100, v[34:35] offset:61440
	s_setprio 1
	s_waitcnt lgkmcnt(1)
	v_mfma_f32_16x16x32_f16 v[32:35], v[108:111], v[170:173], v[206:209]
	v_mfma_f32_16x16x32_f16 v[100:103], v[108:111], v[174:177], v[210:213]
	v_mfma_f32_16x16x32_f16 v[104:107], v[108:111], v[178:181], v[214:217]
	v_mfma_f32_16x16x32_f16 v[108:111], v[108:111], v[182:185], v[150:153]
	v_mfma_f32_16x16x32_f16 v[112:115], v[124:127], v[170:173], v[154:157]
	v_mfma_f32_16x16x32_f16 v[116:119], v[124:127], v[174:177], v[158:161]
	v_mfma_f32_16x16x32_f16 v[120:123], v[124:127], v[178:181], v[166:169]
	v_mfma_f32_16x16x32_f16 v[124:127], v[124:127], v[182:185], v[162:165]
	s_setprio 0
	s_waitcnt vmcnt(0)
	s_waitcnt lgkmcnt(0)
	s_barrier
	ds_read_b128 v[134:137], v131 offset:32768
	ds_read_b128 v[138:141], v131 offset:34816
	ds_read_b128 v[142:145], v131 offset:36864
	ds_read_b128 v[148:151], v131 offset:38912
	ds_read_b128 v[152:155], v129 offset:32768
	ds_read_b128 v[156:159], v129 offset:34816
	s_setprio 1
	s_waitcnt lgkmcnt(0)
	v_mfma_f32_16x16x32_f16 v[0:3], v[152:155], v[134:137], v[0:3]
	v_mfma_f32_16x16x32_f16 v[4:7], v[152:155], v[138:141], v[4:7]
	v_mfma_f32_16x16x32_f16 v[8:11], v[152:155], v[142:145], v[8:11]
	v_mfma_f32_16x16x32_f16 v[12:15], v[152:155], v[148:151], v[12:15]
	v_mfma_f32_16x16x32_f16 v[16:19], v[156:159], v[134:137], v[16:19]
	v_mfma_f32_16x16x32_f16 v[20:23], v[156:159], v[138:141], v[20:23]
	v_mfma_f32_16x16x32_f16 v[36:39], v[156:159], v[142:145], v[36:39]
	v_mfma_f32_16x16x32_f16 v[40:43], v[156:159], v[148:151], v[40:43]
	s_setprio 0
	ds_read_b128 v[152:155], v129 offset:36864
	ds_read_b128 v[156:159], v129 offset:38912
	v_and_b32_e32 v250, 0x7ffffc00, v194
	v_lshl_add_u64 v[252:253], s[10:11], 0, v[196:197]
	v_readfirstlane_b32 s32, v250
	s_nop 0
	s_mov_b32 m0, s32
	s_nop 0
	global_load_lds_dwordx4 v[252:253], off
	v_mov_b32_e32 v146, 0
	v_and_b32_e32 v251, 0xfffffff, v132
	v_cmp_gt_u32_e32 vcc, s82, v251
	v_mov_b32_e32 v132, 0
	v_mov_b32_e32 v133, 0
	s_and_saveexec_b64 s[0:1], vcc
	s_cbranch_execz .LBB1_7
	s_and_b32 s64, s78, 0x7ffffc00
	s_or_b32 s64, s64, s33
	v_or_b32_e32 v132, s64, v251
	v_mov_b32_e32 v133, v195
	v_lshl_add_u64 v[132:133], v[132:133], 2, s[12:13]
	global_load_dword v133, v[132:133], off
	v_or_b32_e32 v132, s33, v251
	v_lshlrev_b32_e32 v132, 2, v132
	global_load_dword v146, v132, s[16:17]
	s_nop 0
	global_load_dword v132, v132, s[14:15]
